# accumulator clearing between GEMM units (and other zero fills): even-aligned VGPR pairs cleared with one v_mov_b64 v[N:N+1], 0 instead of two v_mov_b32 copies of a zero register (1700 pairs; section 7
# baseline (speedup 1.0000x reference)
.LBB0_235:
	s_ashr_i32 s15, s14, 31
	s_lshl_b64 s[36:37], s[14:15], 18
	v_readlane_b32 s38, v254, 44
	v_readlane_b32 s39, v254, 45
	s_add_u32 s36, s38, s36
	s_addc_u32 s37, s39, s37
	s_and_b64 s[38:39], s[34:35], exec
	s_cselect_b32 s15, s37, s41
	s_cselect_b32 s54, s36, s40
	s_ashr_i32 s13, s12, 31
	s_lshl_b64 s[38:39], s[12:13], 18
	s_add_u32 s38, s16, s38
	s_addc_u32 s39, s17, s39
	s_and_b64 s[44:45], s[34:35], exec
	s_cselect_b32 s13, s39, s43
	s_cselect_b32 s55, s38, s42
	s_add_u32 s40, s40, 0x20080
	s_addc_u32 s41, s41, 0
	s_add_u32 s56, s42, 0x100
	v_mov_b32_e32 v64, 0
	s_addc_u32 s57, s43, 0
	s_mov_b32 s58, -2
	v_mov_b32_e32 v65, v64
	v_mov_b64_e32 v[66:67], 0
	v_mov_b64_e32 v[116:117], 0
	v_mov_b64_e32 v[118:119], 0
	v_mov_b64_e32 v[84:85], 0
	v_mov_b64_e32 v[86:87], 0
	v_mov_b64_e32 v[128:129], 0
	v_mov_b64_e32 v[130:131], 0
	v_mov_b64_e32 v[32:33], 0
	v_mov_b64_e32 v[34:35], 0
	v_mov_b64_e32 v[48:49], 0
	v_mov_b64_e32 v[50:51], 0
	v_mov_b64_e32 v[36:37], 0
	v_mov_b64_e32 v[38:39], 0
	v_mov_b64_e32 v[52:53], 0
	v_mov_b64_e32 v[54:55], 0
	v_mov_b64_e32 v[40:41], 0
	v_mov_b64_e32 v[42:43], 0
	v_mov_b64_e32 v[56:57], 0
	v_mov_b64_e32 v[58:59], 0
	v_mov_b64_e32 v[44:45], 0
	v_mov_b64_e32 v[46:47], 0
	v_mov_b64_e32 v[72:73], 0
	v_mov_b64_e32 v[74:75], 0
	v_mov_b64_e32 v[96:97], 0
	v_mov_b64_e32 v[98:99], 0
	v_mov_b64_e32 v[136:137], 0
	v_mov_b64_e32 v[138:139], 0
	v_mov_b64_e32 v[108:109], 0
	v_mov_b64_e32 v[110:111], 0
	v_mov_b64_e32 v[140:141], 0
	v_mov_b64_e32 v[142:143], 0
	v_mov_b64_e32 v[112:113], 0
	v_mov_b64_e32 v[114:115], 0
	v_mov_b64_e32 v[144:145], 0
	v_mov_b64_e32 v[146:147], 0
	v_mov_b64_e32 v[124:125], 0
	v_mov_b64_e32 v[126:127], 0
	v_mov_b64_e32 v[156:157], 0
	v_mov_b64_e32 v[158:159], 0
	v_mov_b64_e32 v[148:149], 0
	v_mov_b64_e32 v[150:151], 0
	v_mov_b64_e32 v[120:121], 0
	v_mov_b64_e32 v[122:123], 0
	v_mov_b64_e32 v[152:153], 0
	v_mov_b64_e32 v[154:155], 0
	v_mov_b64_e32 v[132:133], 0
	v_mov_b64_e32 v[134:135], 0
	v_mov_b32_e32 v88, v64
	s_waitcnt lgkmcnt(0)
	v_mov_b32_e32 v89, v64
	v_mov_b64_e32 v[90:91], 0
	v_mov_b64_e32 v[60:61], 0
	v_mov_b64_e32 v[62:63], 0
	v_mov_b64_e32 v[92:93], 0
	v_mov_b64_e32 v[94:95], 0
	v_mov_b64_e32 v[68:69], 0
	v_mov_b64_e32 v[70:71], 0
	v_mov_b64_e32 v[100:101], 0
	v_mov_b64_e32 v[102:103], 0
	v_mov_b64_e32 v[76:77], 0
	v_mov_b64_e32 v[78:79], 0
	v_mov_b64_e32 v[104:105], 0
	v_mov_b64_e32 v[106:107], 0
	v_mov_b64_e32 v[80:81], 0
	v_mov_b64_e32 v[82:83], 0

.LBB0_814:
	s_ashr_i32 s43, s42, 31
	s_lshl_b64 s[44:45], s[42:43], 18
	s_add_u32 s44, s14, s44
	v_lshlrev_b64 v[2:3], 20, v[166:167]
	s_addc_u32 s45, s15, s45
	v_lshl_add_u64 v[168:169], s[44:45], 0, v[2:3]
	v_cndmask_b32_e64 v167, v1, v169, s[4:5]
	v_cndmask_b32_e64 v220, v0, v168, s[4:5]
	v_mov_b32_e32 v173, v161
	v_mov_b32_e32 v175, v161
	s_mov_b64 s[4:5], 0x100
	v_mov_b32_e32 v64, 0
	v_lshl_add_u64 v[176:177], s[34:35], 0, v[174:175]
	v_lshl_add_u64 v[178:179], s[34:35], 0, v[172:173]
	v_lshl_add_u64 v[180:181], v[0:1], 0, s[4:5]
	s_mov_b32 s43, -2
	s_mov_b64 s[4:5], 0
	v_mov_b32_e32 v65, v64
	v_mov_b64_e32 v[66:67], 0
	v_mov_b64_e32 v[68:69], 0
	v_mov_b64_e32 v[70:71], 0
	v_mov_b64_e32 v[80:81], 0
	v_mov_b64_e32 v[82:83], 0
	v_mov_b64_e32 v[84:85], 0
	v_mov_b64_e32 v[86:87], 0
	v_mov_b64_e32 v[96:97], 0
	v_mov_b64_e32 v[98:99], 0
	v_mov_b64_e32 v[100:101], 0
	v_mov_b64_e32 v[102:103], 0
	v_mov_b64_e32 v[112:113], 0
	v_mov_b64_e32 v[114:115], 0
	v_mov_b64_e32 v[116:117], 0
	v_mov_b64_e32 v[118:119], 0
	v_mov_b64_e32 v[128:129], 0
	v_mov_b64_e32 v[130:131], 0
	v_mov_b64_e32 v[132:133], 0
	v_mov_b64_e32 v[134:135], 0
	v_mov_b64_e32 v[144:145], 0
	v_mov_b64_e32 v[146:147], 0
	v_mov_b64_e32 v[148:149], 0
	v_mov_b64_e32 v[150:151], 0
	v_mov_b64_e32 v[104:105], 0
	v_mov_b64_e32 v[106:107], 0
	v_mov_b64_e32 v[108:109], 0
	v_mov_b64_e32 v[110:111], 0
	v_mov_b64_e32 v[120:121], 0
	v_mov_b64_e32 v[122:123], 0
	v_mov_b64_e32 v[124:125], 0
	v_mov_b64_e32 v[126:127], 0
	v_mov_b64_e32 v[136:137], 0
	v_mov_b64_e32 v[138:139], 0
	v_mov_b64_e32 v[140:141], 0
	v_mov_b64_e32 v[142:143], 0
	v_mov_b64_e32 v[152:153], 0
	v_mov_b64_e32 v[154:155], 0
	v_mov_b64_e32 v[156:157], 0
	v_mov_b64_e32 v[158:159], 0
	v_mov_b64_e32 v[52:53], 0
	v_mov_b64_e32 v[54:55], 0
	v_mov_b64_e32 v[48:49], 0
	v_mov_b64_e32 v[50:51], 0
	v_mov_b64_e32 v[36:37], 0
	v_mov_b64_e32 v[38:39], 0
	v_mov_b64_e32 v[32:33], 0
	v_mov_b64_e32 v[34:35], 0
	v_mov_b64_e32 v[92:93], 0
	v_mov_b64_e32 v[94:95], 0
	v_mov_b64_e32 v[88:89], 0
	v_mov_b64_e32 v[90:91], 0
	v_mov_b64_e32 v[76:77], 0
	v_mov_b64_e32 v[78:79], 0
	v_mov_b64_e32 v[72:73], 0
	v_mov_b64_e32 v[74:75], 0
	v_mov_b64_e32 v[60:61], 0
	v_mov_b64_e32 v[62:63], 0
	v_mov_b64_e32 v[56:57], 0
	v_mov_b64_e32 v[58:59], 0
	v_mov_b64_e32 v[44:45], 0
	v_mov_b64_e32 v[46:47], 0
	v_mov_b64_e32 v[40:41], 0
	v_mov_b64_e32 v[42:43], 0

.LBB0_831:
	s_ashr_i32 s17, s16, 31
	s_lshl_b64 s[26:27], s[16:17], 17
	s_add_u32 s26, s18, s26
	s_addc_u32 s27, s21, s27
	s_and_b64 s[34:35], s[2:3], exec
	s_cselect_b32 s17, s27, s39
	s_cselect_b32 s59, s26, s38
	s_ashr_i32 s25, s24, 31
	s_lshl_b64 s[34:35], s[24:25], 17
	s_add_u32 s34, s22, s34
	s_addc_u32 s35, s23, s35
	s_and_b64 s[40:41], s[2:3], exec
	v_mov_b32_e32 v0, 0
	s_cselect_b32 s25, s35, s37
	s_cselect_b32 s60, s34, s36
	s_mov_b64 s[44:45], 0
	s_mov_b64 s[40:41], -1
	s_mov_b64 s[42:43], 0
	v_mov_b32_e32 v1, v0
	v_mov_b64_e32 v[2:3], 0
	v_mov_b64_e32 v[4:5], 0
	v_mov_b64_e32 v[6:7], 0
	v_mov_b64_e32 v[32:33], 0
	v_mov_b64_e32 v[34:35], 0
	v_mov_b64_e32 v[44:45], 0
	v_mov_b64_e32 v[46:47], 0
	v_mov_b64_e32 v[48:49], 0
	v_mov_b64_e32 v[50:51], 0
	v_mov_b64_e32 v[52:53], 0
	v_mov_b64_e32 v[54:55], 0
	v_mov_b64_e32 v[72:73], 0
	v_mov_b64_e32 v[74:75], 0
	v_mov_b64_e32 v[80:81], 0
	v_mov_b64_e32 v[82:83], 0
	v_mov_b64_e32 v[88:89], 0
	v_mov_b64_e32 v[90:91], 0
	v_mov_b64_e32 v[96:97], 0
	v_mov_b64_e32 v[98:99], 0
	v_mov_b64_e32 v[104:105], 0
	v_mov_b64_e32 v[106:107], 0
	v_mov_b64_e32 v[112:113], 0
	v_mov_b64_e32 v[114:115], 0
	v_mov_b64_e32 v[76:77], 0
	v_mov_b64_e32 v[78:79], 0
	v_mov_b64_e32 v[84:85], 0
	v_mov_b64_e32 v[86:87], 0
	v_mov_b64_e32 v[92:93], 0
	v_mov_b64_e32 v[94:95], 0
	v_mov_b64_e32 v[100:101], 0
	v_mov_b64_e32 v[102:103], 0
	v_mov_b64_e32 v[108:109], 0
	v_mov_b64_e32 v[110:111], 0
	v_mov_b64_e32 v[116:117], 0
	v_mov_b64_e32 v[118:119], 0
	v_mov_b64_e32 v[120:121], 0
	v_mov_b64_e32 v[122:123], 0
	v_mov_b64_e32 v[124:125], 0
	v_mov_b64_e32 v[126:127], 0
	v_mov_b64_e32 v[28:29], 0
	v_mov_b64_e32 v[30:31], 0
	v_mov_b64_e32 v[24:25], 0
	v_mov_b64_e32 v[26:27], 0
	v_mov_b64_e32 v[12:13], 0
	v_mov_b64_e32 v[14:15], 0
	v_mov_b64_e32 v[8:9], 0
	v_mov_b64_e32 v[10:11], 0
	v_mov_b64_e32 v[68:69], 0
	v_mov_b64_e32 v[70:71], 0
	v_mov_b64_e32 v[64:65], 0
	v_mov_b64_e32 v[66:67], 0
	v_mov_b64_e32 v[60:61], 0
	v_mov_b64_e32 v[62:63], 0
	v_mov_b64_e32 v[56:57], 0
	v_mov_b64_e32 v[58:59], 0
	v_mov_b64_e32 v[40:41], 0
	v_mov_b64_e32 v[42:43], 0
	v_mov_b64_e32 v[36:37], 0
	v_mov_b64_e32 v[38:39], 0
	v_mov_b64_e32 v[20:21], 0
	v_mov_b64_e32 v[22:23], 0
	v_mov_b64_e32 v[16:17], 0
	v_mov_b64_e32 v[18:19], 0

.LBB0_912:
	s_ashr_i32 s37, s36, 31
	s_lshl_b64 s[38:39], s[36:37], 17
	v_readlane_b32 s40, v254, 46
	v_readlane_b32 s41, v254, 47
	s_add_u32 s38, s40, s38
	s_addc_u32 s39, s41, s39
	s_and_b64 s[40:41], s[4:5], exec
	s_cselect_b32 s37, s39, s35
	s_cselect_b32 s74, s38, s34
	s_ashr_i32 s25, s24, 31
	s_lshl_b64 s[40:41], s[24:25], 17
	v_ashrrev_i32_e32 v171, 31, v170
	s_add_u32 s40, s21, s40
	v_lshlrev_b64 v[0:1], 19, v[170:171]
	s_addc_u32 s41, s22, s41
	v_lshl_add_u64 v[172:173], s[40:41], 0, v[0:1]
	v_mov_b32_e32 v48, 0
	v_cndmask_b32_e64 v171, v169, v173, s[4:5]
	v_cndmask_b32_e64 v205, v168, v172, s[4:5]
	s_mov_b64 s[44:45], 0
	s_mov_b64 s[40:41], -1
	s_mov_b64 s[42:43], 0
	v_mov_b32_e32 v49, v48
	v_mov_b64_e32 v[50:51], 0
	v_mov_b64_e32 v[60:61], 0
	v_mov_b64_e32 v[62:63], 0
	v_mov_b64_e32 v[76:77], 0
	v_mov_b64_e32 v[78:79], 0
	v_mov_b64_e32 v[84:85], 0
	v_mov_b64_e32 v[86:87], 0
	v_mov_b64_e32 v[88:89], 0
	v_mov_b64_e32 v[90:91], 0
	v_mov_b64_e32 v[96:97], 0
	v_mov_b64_e32 v[98:99], 0
	v_mov_b64_e32 v[112:113], 0
	v_mov_b64_e32 v[114:115], 0
	v_mov_b64_e32 v[116:117], 0
	v_mov_b64_e32 v[118:119], 0
	v_mov_b64_e32 v[128:129], 0
	v_mov_b64_e32 v[130:131], 0
	v_mov_b64_e32 v[132:133], 0
	v_mov_b64_e32 v[134:135], 0
	v_mov_b64_e32 v[144:145], 0
	v_mov_b64_e32 v[146:147], 0
	v_mov_b64_e32 v[148:149], 0
	v_mov_b64_e32 v[150:151], 0
	v_mov_b64_e32 v[104:105], 0
	v_mov_b64_e32 v[106:107], 0
	v_mov_b64_e32 v[108:109], 0
	v_mov_b64_e32 v[110:111], 0
	v_mov_b64_e32 v[120:121], 0
	v_mov_b64_e32 v[122:123], 0
	v_mov_b64_e32 v[124:125], 0
	v_mov_b64_e32 v[126:127], 0
	v_mov_b64_e32 v[136:137], 0
	v_mov_b64_e32 v[138:139], 0
	v_mov_b64_e32 v[140:141], 0
	v_mov_b64_e32 v[142:143], 0
	v_mov_b64_e32 v[152:153], 0
	v_mov_b64_e32 v[154:155], 0
	v_mov_b64_e32 v[156:157], 0
	v_mov_b64_e32 v[158:159], 0
	v_mov_b64_e32 v[68:69], 0
	v_mov_b64_e32 v[70:71], 0
	v_mov_b64_e32 v[56:57], 0
	v_mov_b64_e32 v[58:59], 0
	v_mov_b64_e32 v[44:45], 0
	v_mov_b64_e32 v[46:47], 0
	v_mov_b64_e32 v[36:37], 0
	v_mov_b64_e32 v[38:39], 0
	v_mov_b64_e32 v[100:101], 0
	v_mov_b64_e32 v[102:103], 0
	v_mov_b64_e32 v[92:93], 0
	v_mov_b64_e32 v[94:95], 0
	v_mov_b64_e32 v[80:81], 0
	v_mov_b64_e32 v[82:83], 0
	v_mov_b64_e32 v[72:73], 0
	v_mov_b64_e32 v[74:75], 0
	v_mov_b64_e32 v[64:65], 0
	v_mov_b64_e32 v[66:67], 0
	v_mov_b64_e32 v[52:53], 0
	v_mov_b64_e32 v[54:55], 0
	v_mov_b64_e32 v[40:41], 0
	v_mov_b64_e32 v[42:43], 0
	v_mov_b64_e32 v[32:33], 0
	v_mov_b64_e32 v[34:35], 0

.LBB0_1080:
	s_ashr_i32 s13, s12, 31
	s_lshl_b64 s[16:17], s[12:13], 17
	s_add_u32 s16, s22, s16
	s_addc_u32 s17, s23, s17
	s_and_b64 s[24:25], s[2:3], exec
	s_cselect_b32 s13, s17, s35
	s_cselect_b32 s57, s16, s34
	s_ashr_i32 s11, s10, 31
	s_lshl_b64 s[24:25], s[10:11], 17
	s_add_u32 s24, s28, s24
	s_addc_u32 s25, s29, s25
	s_and_b64 s[36:37], s[2:3], exec
	v_mov_b32_e32 v0, 0
	s_cselect_b32 s11, s25, s27
	s_cselect_b32 s58, s24, s26
	s_mov_b64 s[40:41], 0
	s_mov_b64 s[36:37], -1
	s_mov_b64 s[38:39], 0
	v_mov_b32_e32 v1, v0
	v_mov_b64_e32 v[2:3], 0
	v_mov_b64_e32 v[4:5], 0
	v_mov_b64_e32 v[6:7], 0
	v_mov_b64_e32 v[32:33], 0
	v_mov_b64_e32 v[34:35], 0
	v_mov_b64_e32 v[44:45], 0
	v_mov_b64_e32 v[46:47], 0
	v_mov_b64_e32 v[48:49], 0
	v_mov_b64_e32 v[50:51], 0
	v_mov_b64_e32 v[52:53], 0
	v_mov_b64_e32 v[54:55], 0
	v_mov_b64_e32 v[72:73], 0
	v_mov_b64_e32 v[74:75], 0
	v_mov_b64_e32 v[80:81], 0
	v_mov_b64_e32 v[82:83], 0
	v_mov_b64_e32 v[88:89], 0
	v_mov_b64_e32 v[90:91], 0
	v_mov_b64_e32 v[96:97], 0
	v_mov_b64_e32 v[98:99], 0
	v_mov_b64_e32 v[104:105], 0
	v_mov_b64_e32 v[106:107], 0
	v_mov_b64_e32 v[112:113], 0
	v_mov_b64_e32 v[114:115], 0
	v_mov_b64_e32 v[76:77], 0
	v_mov_b64_e32 v[78:79], 0
	v_mov_b64_e32 v[84:85], 0
	v_mov_b64_e32 v[86:87], 0
	v_mov_b64_e32 v[92:93], 0
	v_mov_b64_e32 v[94:95], 0
	v_mov_b64_e32 v[100:101], 0
	v_mov_b64_e32 v[102:103], 0
	v_mov_b64_e32 v[108:109], 0
	v_mov_b64_e32 v[110:111], 0
	v_mov_b64_e32 v[116:117], 0
	v_mov_b64_e32 v[118:119], 0
	v_mov_b64_e32 v[120:121], 0
	v_mov_b64_e32 v[122:123], 0
	v_mov_b64_e32 v[124:125], 0
	v_mov_b64_e32 v[126:127], 0
	v_mov_b64_e32 v[28:29], 0
	v_mov_b64_e32 v[30:31], 0
	v_mov_b64_e32 v[24:25], 0
	v_mov_b64_e32 v[26:27], 0
	v_mov_b64_e32 v[12:13], 0
	v_mov_b64_e32 v[14:15], 0
	v_mov_b64_e32 v[8:9], 0
	v_mov_b64_e32 v[10:11], 0
	v_mov_b64_e32 v[68:69], 0
	v_mov_b64_e32 v[70:71], 0
	v_mov_b64_e32 v[64:65], 0
	v_mov_b64_e32 v[66:67], 0
	v_mov_b64_e32 v[60:61], 0
	v_mov_b64_e32 v[62:63], 0
	v_mov_b64_e32 v[56:57], 0
	v_mov_b64_e32 v[58:59], 0
	v_mov_b64_e32 v[40:41], 0
	v_mov_b64_e32 v[42:43], 0
	v_mov_b64_e32 v[36:37], 0
	v_mov_b64_e32 v[38:39], 0
	v_mov_b64_e32 v[20:21], 0
	v_mov_b64_e32 v[22:23], 0
	v_mov_b64_e32 v[16:17], 0
	v_mov_b64_e32 v[18:19], 0

.LBB0_1101:
	s_ashr_i32 s13, s12, 31
	s_lshl_b64 s[16:17], s[12:13], 19
	s_add_u32 s16, s0, s16
	s_addc_u32 s17, s1, s17
	s_and_b64 s[24:25], s[14:15], exec
	s_cselect_b32 s13, s17, s35
	s_cselect_b32 s44, s16, s34
	s_ashr_i32 s11, s10, 31
	s_lshl_b64 s[24:25], s[10:11], 19
	s_add_u32 s24, s18, s24
	s_addc_u32 s25, s19, s25
	s_and_b64 s[38:39], s[14:15], exec
	s_cselect_b32 s11, s25, s37
	s_cselect_b32 s45, s24, s36
	s_add_u32 s34, s34, 0x40080
	s_addc_u32 s35, s35, 0
	s_add_u32 s46, s36, 0x100
	v_mov_b32_e32 v36, 0
	s_addc_u32 s47, s37, 0
	s_mov_b32 s48, -2
	v_mov_b32_e32 v37, v36
	v_mov_b64_e32 v[38:39], 0
	v_mov_b64_e32 v[44:45], 0
	v_mov_b64_e32 v[46:47], 0
	v_mov_b64_e32 v[52:53], 0
	v_mov_b64_e32 v[54:55], 0
	v_mov_b64_e32 v[60:61], 0
	v_mov_b64_e32 v[62:63], 0
	v_mov_b64_e32 v[64:65], 0
	v_mov_b64_e32 v[66:67], 0
	v_mov_b64_e32 v[68:69], 0
	v_mov_b64_e32 v[70:71], 0
	v_mov_b64_e32 v[80:81], 0
	v_mov_b64_e32 v[82:83], 0
	v_mov_b64_e32 v[84:85], 0
	v_mov_b64_e32 v[86:87], 0
	v_mov_b64_e32 v[96:97], 0
	v_mov_b64_e32 v[98:99], 0
	v_mov_b64_e32 v[100:101], 0
	v_mov_b64_e32 v[102:103], 0
	v_mov_b64_e32 v[112:113], 0
	v_mov_b64_e32 v[114:115], 0
	v_mov_b64_e32 v[116:117], 0
	v_mov_b64_e32 v[118:119], 0
	v_mov_b64_e32 v[72:73], 0
	v_mov_b64_e32 v[74:75], 0
	v_mov_b64_e32 v[76:77], 0
	v_mov_b64_e32 v[78:79], 0
	v_mov_b64_e32 v[88:89], 0
	v_mov_b64_e32 v[90:91], 0
	v_mov_b64_e32 v[92:93], 0
	v_mov_b64_e32 v[94:95], 0
	v_mov_b64_e32 v[104:105], 0
	v_mov_b64_e32 v[106:107], 0
	v_mov_b64_e32 v[108:109], 0
	v_mov_b64_e32 v[110:111], 0
	v_mov_b64_e32 v[128:129], 0
	v_mov_b64_e32 v[130:131], 0
	v_mov_b64_e32 v[120:121], 0
	v_mov_b64_e32 v[122:123], 0
	v_mov_b64_e32 v[28:29], 0
	v_mov_b64_e32 v[30:31], 0
	v_mov_b64_e32 v[24:25], 0
	v_mov_b64_e32 v[26:27], 0
	v_mov_b64_e32 v[12:13], 0
	v_mov_b64_e32 v[14:15], 0
	v_mov_b64_e32 v[8:9], 0
	v_mov_b64_e32 v[10:11], 0
	v_mov_b64_e32 v[56:57], 0
	v_mov_b64_e32 v[58:59], 0
	v_mov_b64_e32 v[48:49], 0
	v_mov_b64_e32 v[50:51], 0
	v_mov_b64_e32 v[40:41], 0
	v_mov_b64_e32 v[42:43], 0
	s_waitcnt vmcnt(0)
	v_mov_b64_e32 v[32:33], 0
	v_mov_b64_e32 v[34:35], 0
	v_mov_b64_e32 v[20:21], 0
	v_mov_b64_e32 v[22:23], 0
	v_mov_b64_e32 v[16:17], 0
	v_mov_b64_e32 v[18:19], 0
	v_mov_b64_e32 v[4:5], 0
	v_mov_b64_e32 v[6:7], 0
	v_mov_b64_e32 v[0:1], 0
	v_mov_b64_e32 v[2:3], 0

.LBB0_1174:
	s_ashr_i32 s9, s8, 31
	s_lshl_b64 s[12:13], s[8:9], 18
	v_readlane_b32 s14, v254, 44
	v_readlane_b32 s15, v254, 45
	s_add_u32 s12, s14, s12
	s_addc_u32 s13, s15, s13
	s_and_b64 s[14:15], s[10:11], exec
	s_cselect_b32 s9, s13, s25
	s_cselect_b32 s46, s12, s24
	s_ashr_i32 s7, s6, 31
	s_lshl_b64 s[14:15], s[6:7], 18
	s_add_u32 s14, s18, s14
	s_addc_u32 s15, s19, s15
	s_and_b64 s[34:35], s[10:11], exec
	s_cselect_b32 s7, s15, s27
	s_cselect_b32 s47, s14, s26
	s_add_u32 s24, s24, 0x20080
	s_addc_u32 s25, s25, 0
	s_add_u32 s48, s26, 0x100
	v_mov_b32_e32 v48, 0
	s_addc_u32 s49, s27, 0
	s_mov_b32 s50, -2
	v_mov_b32_e32 v49, v48
	v_mov_b64_e32 v[50:51], 0
	v_mov_b64_e32 v[52:53], 0
	v_mov_b64_e32 v[54:55], 0
	v_mov_b64_e32 v[72:73], 0
	v_mov_b64_e32 v[74:75], 0
	v_mov_b64_e32 v[76:77], 0
	v_mov_b64_e32 v[78:79], 0
	v_mov_b64_e32 v[88:89], 0
	v_mov_b64_e32 v[90:91], 0
	v_mov_b64_e32 v[92:93], 0
	v_mov_b64_e32 v[94:95], 0
	v_mov_b64_e32 v[108:109], 0
	v_mov_b64_e32 v[110:111], 0
	v_mov_b64_e32 v[116:117], 0
	v_mov_b64_e32 v[118:119], 0
	v_mov_b64_e32 v[124:125], 0
	v_mov_b64_e32 v[126:127], 0
	v_mov_b64_e32 v[132:133], 0
	v_mov_b64_e32 v[134:135], 0
	v_mov_b64_e32 v[140:141], 0
	v_mov_b64_e32 v[142:143], 0
	v_mov_b64_e32 v[148:149], 0
	v_mov_b64_e32 v[150:151], 0
	v_mov_b64_e32 v[104:105], 0
	v_mov_b64_e32 v[106:107], 0
	v_mov_b64_e32 v[112:113], 0
	v_mov_b64_e32 v[114:115], 0
	v_mov_b64_e32 v[120:121], 0
	v_mov_b64_e32 v[122:123], 0
	v_mov_b64_e32 v[128:129], 0
	v_mov_b64_e32 v[130:131], 0
	v_mov_b64_e32 v[136:137], 0
	v_mov_b64_e32 v[138:139], 0
	v_mov_b64_e32 v[144:145], 0
	v_mov_b64_e32 v[146:147], 0
	v_mov_b64_e32 v[152:153], 0
	v_mov_b64_e32 v[154:155], 0
	v_mov_b64_e32 v[156:157], 0
	v_mov_b64_e32 v[158:159], 0
	v_mov_b64_e32 v[60:61], 0
	v_mov_b64_e32 v[62:63], 0
	v_mov_b64_e32 v[56:57], 0
	v_mov_b64_e32 v[58:59], 0
	v_mov_b64_e32 v[36:37], 0
	v_mov_b64_e32 v[38:39], 0
	v_mov_b64_e32 v[32:33], 0
	v_mov_b64_e32 v[34:35], 0
	v_mov_b64_e32 v[100:101], 0
	v_mov_b64_e32 v[102:103], 0
	v_mov_b64_e32 v[96:97], 0
	v_mov_b64_e32 v[98:99], 0
	v_mov_b64_e32 v[84:85], 0
	v_mov_b64_e32 v[86:87], 0
	v_mov_b64_e32 v[80:81], 0
	v_mov_b64_e32 v[82:83], 0
	v_mov_b64_e32 v[68:69], 0
	v_mov_b64_e32 v[70:71], 0
	v_mov_b64_e32 v[64:65], 0
	v_mov_b64_e32 v[66:67], 0
	v_mov_b64_e32 v[44:45], 0
	v_mov_b64_e32 v[46:47], 0
	v_mov_b64_e32 v[40:41], 0
	v_mov_b64_e32 v[42:43], 0

.LBB0_1500:
	s_ashr_i32 s43, s42, 31
	s_lshl_b64 s[48:49], s[42:43], 18
	v_readlane_b32 s1, v254, 48
	s_add_u32 s48, s1, s48
	v_readlane_b32 s1, v254, 49
	s_addc_u32 s49, s1, s49
	s_and_b64 s[50:51], s[46:47], exec
	s_cselect_b32 s1, s49, s3
	s_cselect_b32 s5, s48, s2
	s_ashr_i32 s45, s44, 31
	s_lshl_b64 s[50:51], s[44:45], 18
	s_add_u32 s50, s41, s50
	s_addc_u32 s51, s60, s51
	s_and_b64 s[52:53], s[46:47], exec
	s_cselect_b32 s33, s51, s7
	s_cselect_b32 s43, s50, s6
	s_add_u32 s2, s2, 0x20080
	s_addc_u32 s3, s3, 0
	s_add_u32 s45, s6, 0x100
	v_mov_b32_e32 v64, 0
	s_addc_u32 s54, s7, 0
	s_mov_b32 s55, -2
	v_mov_b32_e32 v65, v64
	v_mov_b64_e32 v[66:67], 0
	v_mov_b64_e32 v[68:69], 0
	v_mov_b64_e32 v[70:71], 0
	v_mov_b64_e32 v[80:81], 0
	v_mov_b64_e32 v[82:83], 0
	v_mov_b64_e32 v[84:85], 0
	v_mov_b64_e32 v[86:87], 0
	v_mov_b64_e32 v[96:97], 0
	v_mov_b64_e32 v[98:99], 0
	v_mov_b64_e32 v[100:101], 0
	v_mov_b64_e32 v[102:103], 0
	v_mov_b64_e32 v[112:113], 0
	v_mov_b64_e32 v[114:115], 0
	v_mov_b64_e32 v[116:117], 0
	v_mov_b64_e32 v[118:119], 0
	v_mov_b64_e32 v[128:129], 0
	v_mov_b64_e32 v[130:131], 0
	v_mov_b64_e32 v[132:133], 0
	v_mov_b64_e32 v[134:135], 0
	v_mov_b64_e32 v[144:145], 0
	v_mov_b64_e32 v[146:147], 0
	v_mov_b64_e32 v[148:149], 0
	v_mov_b64_e32 v[150:151], 0
	v_mov_b64_e32 v[104:105], 0
	v_mov_b64_e32 v[106:107], 0
	v_mov_b64_e32 v[108:109], 0
	v_mov_b64_e32 v[110:111], 0
	v_mov_b64_e32 v[120:121], 0
	v_mov_b64_e32 v[122:123], 0
	v_mov_b64_e32 v[124:125], 0
	v_mov_b64_e32 v[126:127], 0
	v_mov_b64_e32 v[136:137], 0
	v_mov_b64_e32 v[138:139], 0
	v_mov_b64_e32 v[140:141], 0
	v_mov_b64_e32 v[142:143], 0
	v_mov_b64_e32 v[152:153], 0
	v_mov_b64_e32 v[154:155], 0
	v_mov_b64_e32 v[156:157], 0
	v_mov_b64_e32 v[158:159], 0
	v_mov_b64_e32 v[56:57], 0
	v_mov_b64_e32 v[58:59], 0
	v_mov_b64_e32 v[48:49], 0
	v_mov_b64_e32 v[50:51], 0
	v_mov_b64_e32 v[40:41], 0
	v_mov_b64_e32 v[42:43], 0
	s_waitcnt vmcnt(0)
	v_mov_b64_e32 v[32:33], 0
	v_mov_b64_e32 v[34:35], 0
	v_mov_b64_e32 v[92:93], 0
	v_mov_b64_e32 v[94:95], 0
	v_mov_b64_e32 v[88:89], 0
	v_mov_b64_e32 v[90:91], 0
	v_mov_b64_e32 v[76:77], 0
	v_mov_b64_e32 v[78:79], 0
	v_mov_b64_e32 v[72:73], 0
	v_mov_b64_e32 v[74:75], 0
	v_mov_b64_e32 v[60:61], 0
	v_mov_b64_e32 v[62:63], 0
	v_mov_b64_e32 v[52:53], 0
	v_mov_b64_e32 v[54:55], 0
	v_mov_b64_e32 v[44:45], 0
	v_mov_b64_e32 v[46:47], 0
	v_mov_b64_e32 v[36:37], 0
	v_mov_b64_e32 v[38:39], 0

.LBB0_1691:
	s_ashr_i32 s41, s40, 31
	s_lshl_b64 s[42:43], s[40:41], 18
	s_add_u32 s42, s10, s42
	v_lshlrev_b64 v[2:3], 20, v[166:167]
	s_addc_u32 s43, s11, s43
	v_lshl_add_u64 v[168:169], s[42:43], 0, v[2:3]
	v_cndmask_b32_e64 v167, v1, v169, s[4:5]
	v_cndmask_b32_e64 v220, v0, v168, s[4:5]
	v_mov_b32_e32 v173, v161
	v_mov_b32_e32 v175, v161
	s_mov_b64 s[4:5], 0x100
	v_mov_b32_e32 v64, 0
	v_lshl_add_u64 v[176:177], s[30:31], 0, v[174:175]
	v_lshl_add_u64 v[178:179], s[30:31], 0, v[172:173]
	v_lshl_add_u64 v[180:181], v[0:1], 0, s[4:5]
	s_mov_b32 s41, -2
	s_mov_b64 s[4:5], 0
	v_mov_b32_e32 v65, v64
	v_mov_b64_e32 v[66:67], 0
	v_mov_b64_e32 v[68:69], 0
	v_mov_b64_e32 v[70:71], 0
	v_mov_b64_e32 v[80:81], 0
	v_mov_b64_e32 v[82:83], 0
	v_mov_b64_e32 v[84:85], 0
	v_mov_b64_e32 v[86:87], 0
	v_mov_b64_e32 v[96:97], 0
	v_mov_b64_e32 v[98:99], 0
	v_mov_b64_e32 v[100:101], 0
	v_mov_b64_e32 v[102:103], 0
	v_mov_b64_e32 v[112:113], 0
	v_mov_b64_e32 v[114:115], 0
	v_mov_b64_e32 v[116:117], 0
	v_mov_b64_e32 v[118:119], 0
	v_mov_b64_e32 v[128:129], 0
	v_mov_b64_e32 v[130:131], 0
	v_mov_b64_e32 v[132:133], 0
	v_mov_b64_e32 v[134:135], 0
	v_mov_b64_e32 v[144:145], 0
	v_mov_b64_e32 v[146:147], 0
	v_mov_b64_e32 v[148:149], 0
	v_mov_b64_e32 v[150:151], 0
	v_mov_b64_e32 v[104:105], 0
	v_mov_b64_e32 v[106:107], 0
	v_mov_b64_e32 v[108:109], 0
	v_mov_b64_e32 v[110:111], 0
	v_mov_b64_e32 v[120:121], 0
	v_mov_b64_e32 v[122:123], 0
	v_mov_b64_e32 v[124:125], 0
	v_mov_b64_e32 v[126:127], 0
	v_mov_b64_e32 v[136:137], 0
	v_mov_b64_e32 v[138:139], 0
	v_mov_b64_e32 v[140:141], 0
	v_mov_b64_e32 v[142:143], 0
	v_mov_b64_e32 v[152:153], 0
	v_mov_b64_e32 v[154:155], 0
	v_mov_b64_e32 v[156:157], 0
	v_mov_b64_e32 v[158:159], 0
	v_mov_b64_e32 v[52:53], 0
	v_mov_b64_e32 v[54:55], 0
	v_mov_b64_e32 v[48:49], 0
	v_mov_b64_e32 v[50:51], 0
	v_mov_b64_e32 v[36:37], 0
	v_mov_b64_e32 v[38:39], 0
	v_mov_b64_e32 v[32:33], 0
	v_mov_b64_e32 v[34:35], 0
	v_mov_b64_e32 v[92:93], 0
	v_mov_b64_e32 v[94:95], 0
	v_mov_b64_e32 v[88:89], 0
	v_mov_b64_e32 v[90:91], 0
	v_mov_b64_e32 v[76:77], 0
	v_mov_b64_e32 v[78:79], 0
	v_mov_b64_e32 v[72:73], 0
	v_mov_b64_e32 v[74:75], 0
	v_mov_b64_e32 v[60:61], 0
	v_mov_b64_e32 v[62:63], 0
	v_mov_b64_e32 v[56:57], 0
	v_mov_b64_e32 v[58:59], 0
	v_mov_b64_e32 v[44:45], 0
	v_mov_b64_e32 v[46:47], 0
	v_mov_b64_e32 v[40:41], 0
	v_mov_b64_e32 v[42:43], 0

.LBB0_1708:
	s_ashr_i32 s13, s12, 31
	s_lshl_b64 s[16:17], s[12:13], 17
	s_add_u32 s16, s18, s16
	s_addc_u32 s17, s21, s17
	s_and_b64 s[30:31], s[2:3], exec
	s_cselect_b32 s13, s17, s37
	s_cselect_b32 s61, s16, s36
	s_ashr_i32 s15, s14, 31
	s_lshl_b64 s[30:31], s[14:15], 17
	s_add_u32 s30, s22, s30
	s_addc_u32 s31, s23, s31
	s_and_b64 s[38:39], s[2:3], exec
	v_mov_b32_e32 v0, 0
	s_cselect_b32 s15, s31, s35
	s_cselect_b32 s62, s30, s34
	s_mov_b64 s[42:43], 0
	s_mov_b64 s[38:39], -1
	s_mov_b64 s[40:41], 0
	v_mov_b32_e32 v1, v0
	v_mov_b64_e32 v[2:3], 0
	v_mov_b64_e32 v[4:5], 0
	v_mov_b64_e32 v[6:7], 0
	v_mov_b64_e32 v[32:33], 0
	v_mov_b64_e32 v[34:35], 0
	v_mov_b64_e32 v[44:45], 0
	v_mov_b64_e32 v[46:47], 0
	v_mov_b64_e32 v[48:49], 0
	v_mov_b64_e32 v[50:51], 0
	v_mov_b64_e32 v[52:53], 0
	v_mov_b64_e32 v[54:55], 0
	v_mov_b64_e32 v[72:73], 0
	v_mov_b64_e32 v[74:75], 0
	v_mov_b64_e32 v[80:81], 0
	v_mov_b64_e32 v[82:83], 0
	v_mov_b64_e32 v[88:89], 0
	v_mov_b64_e32 v[90:91], 0
	v_mov_b64_e32 v[96:97], 0
	v_mov_b64_e32 v[98:99], 0
	v_mov_b64_e32 v[104:105], 0
	v_mov_b64_e32 v[106:107], 0
	v_mov_b64_e32 v[112:113], 0
	v_mov_b64_e32 v[114:115], 0
	v_mov_b64_e32 v[76:77], 0
	v_mov_b64_e32 v[78:79], 0
	v_mov_b64_e32 v[84:85], 0
	v_mov_b64_e32 v[86:87], 0
	v_mov_b64_e32 v[92:93], 0
	v_mov_b64_e32 v[94:95], 0
	v_mov_b64_e32 v[100:101], 0
	v_mov_b64_e32 v[102:103], 0
	v_mov_b64_e32 v[108:109], 0
	v_mov_b64_e32 v[110:111], 0
	v_mov_b64_e32 v[116:117], 0
	v_mov_b64_e32 v[118:119], 0
	v_mov_b64_e32 v[120:121], 0
	v_mov_b64_e32 v[122:123], 0
	v_mov_b64_e32 v[124:125], 0
	v_mov_b64_e32 v[126:127], 0
	v_mov_b64_e32 v[28:29], 0
	v_mov_b64_e32 v[30:31], 0
	v_mov_b64_e32 v[24:25], 0
	v_mov_b64_e32 v[26:27], 0
	v_mov_b64_e32 v[12:13], 0
	v_mov_b64_e32 v[14:15], 0
	v_mov_b64_e32 v[8:9], 0
	v_mov_b64_e32 v[10:11], 0
	v_mov_b64_e32 v[68:69], 0
	v_mov_b64_e32 v[70:71], 0
	v_mov_b64_e32 v[64:65], 0
	v_mov_b64_e32 v[66:67], 0
	v_mov_b64_e32 v[60:61], 0
	v_mov_b64_e32 v[62:63], 0
	v_mov_b64_e32 v[56:57], 0
	v_mov_b64_e32 v[58:59], 0
	v_mov_b64_e32 v[40:41], 0
	v_mov_b64_e32 v[42:43], 0
	v_mov_b64_e32 v[36:37], 0
	v_mov_b64_e32 v[38:39], 0
	v_mov_b64_e32 v[20:21], 0
	v_mov_b64_e32 v[22:23], 0
	v_mov_b64_e32 v[16:17], 0
	v_mov_b64_e32 v[18:19], 0

.LBB0_1789:
	s_ashr_i32 s35, s34, 31
	s_lshl_b64 s[36:37], s[34:35], 17
	v_readlane_b32 s38, v254, 46
	v_readlane_b32 s39, v254, 47
	s_add_u32 s36, s38, s36
	s_addc_u32 s37, s39, s37
	s_and_b64 s[38:39], s[4:5], exec
	s_cselect_b32 s35, s37, s31
	s_cselect_b32 s92, s36, s30
	s_ashr_i32 s15, s14, 31
	s_lshl_b64 s[38:39], s[14:15], 17
	v_ashrrev_i32_e32 v171, 31, v170
	s_add_u32 s38, s17, s38
	v_lshlrev_b64 v[0:1], 19, v[170:171]
	s_addc_u32 s39, s21, s39
	v_lshl_add_u64 v[172:173], s[38:39], 0, v[0:1]
	v_mov_b32_e32 v48, 0
	v_cndmask_b32_e64 v171, v169, v173, s[4:5]
	v_cndmask_b32_e64 v205, v168, v172, s[4:5]
	s_mov_b64 s[42:43], 0
	s_mov_b64 s[38:39], -1
	s_mov_b64 s[40:41], 0
	v_mov_b32_e32 v49, v48
	v_mov_b64_e32 v[50:51], 0
	v_mov_b64_e32 v[60:61], 0
	v_mov_b64_e32 v[62:63], 0
	v_mov_b64_e32 v[76:77], 0
	v_mov_b64_e32 v[78:79], 0
	v_mov_b64_e32 v[84:85], 0
	v_mov_b64_e32 v[86:87], 0
	v_mov_b64_e32 v[88:89], 0
	v_mov_b64_e32 v[90:91], 0
	v_mov_b64_e32 v[96:97], 0
	v_mov_b64_e32 v[98:99], 0
	v_mov_b64_e32 v[112:113], 0
	v_mov_b64_e32 v[114:115], 0
	v_mov_b64_e32 v[116:117], 0
	v_mov_b64_e32 v[118:119], 0
	v_mov_b64_e32 v[128:129], 0
	v_mov_b64_e32 v[130:131], 0
	v_mov_b64_e32 v[132:133], 0
	v_mov_b64_e32 v[134:135], 0
	v_mov_b64_e32 v[144:145], 0
	v_mov_b64_e32 v[146:147], 0
	v_mov_b64_e32 v[148:149], 0
	v_mov_b64_e32 v[150:151], 0
	v_mov_b64_e32 v[104:105], 0
	v_mov_b64_e32 v[106:107], 0
	v_mov_b64_e32 v[108:109], 0
	v_mov_b64_e32 v[110:111], 0
	v_mov_b64_e32 v[120:121], 0
	v_mov_b64_e32 v[122:123], 0
	v_mov_b64_e32 v[124:125], 0
	v_mov_b64_e32 v[126:127], 0
	v_mov_b64_e32 v[136:137], 0
	v_mov_b64_e32 v[138:139], 0
	v_mov_b64_e32 v[140:141], 0
	v_mov_b64_e32 v[142:143], 0
	v_mov_b64_e32 v[152:153], 0
	v_mov_b64_e32 v[154:155], 0
	v_mov_b64_e32 v[156:157], 0
	v_mov_b64_e32 v[158:159], 0
	v_mov_b64_e32 v[68:69], 0
	v_mov_b64_e32 v[70:71], 0
	v_mov_b64_e32 v[56:57], 0
	v_mov_b64_e32 v[58:59], 0
	v_mov_b64_e32 v[44:45], 0
	v_mov_b64_e32 v[46:47], 0
	v_mov_b64_e32 v[36:37], 0
	v_mov_b64_e32 v[38:39], 0
	v_mov_b64_e32 v[100:101], 0
	v_mov_b64_e32 v[102:103], 0
	v_mov_b64_e32 v[92:93], 0
	v_mov_b64_e32 v[94:95], 0
	v_mov_b64_e32 v[80:81], 0
	v_mov_b64_e32 v[82:83], 0
	v_mov_b64_e32 v[72:73], 0
	v_mov_b64_e32 v[74:75], 0
	v_mov_b64_e32 v[64:65], 0
	v_mov_b64_e32 v[66:67], 0
	v_mov_b64_e32 v[52:53], 0
	v_mov_b64_e32 v[54:55], 0
	v_mov_b64_e32 v[40:41], 0
	v_mov_b64_e32 v[42:43], 0
	v_mov_b64_e32 v[32:33], 0
	v_mov_b64_e32 v[34:35], 0

.LBB0_1957:
	s_ashr_i32 s11, s10, 31
	s_lshl_b64 s[12:13], s[10:11], 17
	s_add_u32 s12, s22, s12
	s_addc_u32 s13, s23, s13
	s_and_b64 s[16:17], s[2:3], exec
	s_cselect_b32 s11, s13, s31
	s_cselect_b32 s59, s12, s30
	s_ashr_i32 s9, s8, 31
	s_lshl_b64 s[16:17], s[8:9], 17
	s_add_u32 s16, s33, s16
	s_addc_u32 s17, s48, s17
	s_and_b64 s[34:35], s[2:3], exec
	v_mov_b32_e32 v0, 0
	s_cselect_b32 s9, s17, s29
	s_cselect_b32 s60, s16, s28
	s_mov_b64 s[38:39], 0
	s_mov_b64 s[34:35], -1
	s_mov_b64 s[36:37], 0
	v_mov_b32_e32 v1, v0
	v_mov_b64_e32 v[2:3], 0
	v_mov_b64_e32 v[4:5], 0
	v_mov_b64_e32 v[6:7], 0
	v_mov_b64_e32 v[32:33], 0
	v_mov_b64_e32 v[34:35], 0
	v_mov_b64_e32 v[44:45], 0
	v_mov_b64_e32 v[46:47], 0
	v_mov_b64_e32 v[48:49], 0
	v_mov_b64_e32 v[50:51], 0
	v_mov_b64_e32 v[52:53], 0
	v_mov_b64_e32 v[54:55], 0
	v_mov_b64_e32 v[72:73], 0
	v_mov_b64_e32 v[74:75], 0
	v_mov_b64_e32 v[80:81], 0
	v_mov_b64_e32 v[82:83], 0
	v_mov_b64_e32 v[88:89], 0
	v_mov_b64_e32 v[90:91], 0
	v_mov_b64_e32 v[96:97], 0
	v_mov_b64_e32 v[98:99], 0
	v_mov_b64_e32 v[104:105], 0
	v_mov_b64_e32 v[106:107], 0
	v_mov_b64_e32 v[112:113], 0
	v_mov_b64_e32 v[114:115], 0
	v_mov_b64_e32 v[76:77], 0
	v_mov_b64_e32 v[78:79], 0
	v_mov_b64_e32 v[84:85], 0
	v_mov_b64_e32 v[86:87], 0
	v_mov_b64_e32 v[92:93], 0
	v_mov_b64_e32 v[94:95], 0
	v_mov_b64_e32 v[100:101], 0
	v_mov_b64_e32 v[102:103], 0
	v_mov_b64_e32 v[108:109], 0
	v_mov_b64_e32 v[110:111], 0
	v_mov_b64_e32 v[116:117], 0
	v_mov_b64_e32 v[118:119], 0
	v_mov_b64_e32 v[120:121], 0
	v_mov_b64_e32 v[122:123], 0
	v_mov_b64_e32 v[124:125], 0
	v_mov_b64_e32 v[126:127], 0
	v_mov_b64_e32 v[28:29], 0
	v_mov_b64_e32 v[30:31], 0
	v_mov_b64_e32 v[24:25], 0
	v_mov_b64_e32 v[26:27], 0
	v_mov_b64_e32 v[12:13], 0
	v_mov_b64_e32 v[14:15], 0
	v_mov_b64_e32 v[8:9], 0
	v_mov_b64_e32 v[10:11], 0
	v_mov_b64_e32 v[68:69], 0
	v_mov_b64_e32 v[70:71], 0
	v_mov_b64_e32 v[64:65], 0
	v_mov_b64_e32 v[66:67], 0
	v_mov_b64_e32 v[60:61], 0
	v_mov_b64_e32 v[62:63], 0
	v_mov_b64_e32 v[56:57], 0
	v_mov_b64_e32 v[58:59], 0
	v_mov_b64_e32 v[40:41], 0
	v_mov_b64_e32 v[42:43], 0
	v_mov_b64_e32 v[36:37], 0
	v_mov_b64_e32 v[38:39], 0
	v_mov_b64_e32 v[20:21], 0
	v_mov_b64_e32 v[22:23], 0
	v_mov_b64_e32 v[16:17], 0
	v_mov_b64_e32 v[18:19], 0

.LBB0_1978:
	s_ashr_i32 s9, s8, 31
	s_lshl_b64 s[12:13], s[8:9], 19
	s_add_u32 s12, s24, s12
	s_addc_u32 s13, s25, s13
	s_and_b64 s[14:15], s[10:11], exec
	s_cselect_b32 s9, s13, s29
	s_cselect_b32 s44, s12, s28
	s_ashr_i32 s7, s6, 31
	s_lshl_b64 s[14:15], s[6:7], 19
	s_add_u32 s14, s18, s14
	s_addc_u32 s15, s19, s15
	s_and_b64 s[34:35], s[10:11], exec
	s_cselect_b32 s7, s15, s31
	s_cselect_b32 s45, s14, s30
	s_add_u32 s28, s28, 0x40080
	s_addc_u32 s29, s29, 0
	s_add_u32 s46, s30, 0x100
	v_mov_b32_e32 v36, 0
	s_addc_u32 s47, s31, 0
	s_mov_b32 s48, -2
	v_mov_b32_e32 v37, v36
	v_mov_b64_e32 v[38:39], 0
	v_mov_b64_e32 v[44:45], 0
	v_mov_b64_e32 v[46:47], 0
	v_mov_b64_e32 v[52:53], 0
	v_mov_b64_e32 v[54:55], 0
	v_mov_b64_e32 v[60:61], 0
	v_mov_b64_e32 v[62:63], 0
	v_mov_b64_e32 v[64:65], 0
	v_mov_b64_e32 v[66:67], 0
	v_mov_b64_e32 v[68:69], 0
	v_mov_b64_e32 v[70:71], 0
	v_mov_b64_e32 v[80:81], 0
	v_mov_b64_e32 v[82:83], 0
	v_mov_b64_e32 v[84:85], 0
	v_mov_b64_e32 v[86:87], 0
	v_mov_b64_e32 v[96:97], 0
	v_mov_b64_e32 v[98:99], 0
	v_mov_b64_e32 v[100:101], 0
	v_mov_b64_e32 v[102:103], 0
	v_mov_b64_e32 v[112:113], 0
	v_mov_b64_e32 v[114:115], 0
	v_mov_b64_e32 v[116:117], 0
	v_mov_b64_e32 v[118:119], 0
	v_mov_b64_e32 v[72:73], 0
	v_mov_b64_e32 v[74:75], 0
	v_mov_b64_e32 v[76:77], 0
	v_mov_b64_e32 v[78:79], 0
	v_mov_b64_e32 v[88:89], 0
	v_mov_b64_e32 v[90:91], 0
	v_mov_b64_e32 v[92:93], 0
	v_mov_b64_e32 v[94:95], 0
	v_mov_b64_e32 v[104:105], 0
	v_mov_b64_e32 v[106:107], 0
	v_mov_b64_e32 v[108:109], 0
	v_mov_b64_e32 v[110:111], 0
	v_mov_b64_e32 v[128:129], 0
	v_mov_b64_e32 v[130:131], 0
	v_mov_b64_e32 v[120:121], 0
	v_mov_b64_e32 v[122:123], 0
	v_mov_b64_e32 v[28:29], 0
	v_mov_b64_e32 v[30:31], 0
	v_mov_b64_e32 v[24:25], 0
	v_mov_b64_e32 v[26:27], 0
	v_mov_b64_e32 v[12:13], 0
	v_mov_b64_e32 v[14:15], 0
	v_mov_b64_e32 v[8:9], 0
	v_mov_b64_e32 v[10:11], 0
	v_mov_b64_e32 v[56:57], 0
	v_mov_b64_e32 v[58:59], 0
	v_mov_b64_e32 v[48:49], 0
	v_mov_b64_e32 v[50:51], 0
	v_mov_b64_e32 v[40:41], 0
	v_mov_b64_e32 v[42:43], 0
	s_waitcnt vmcnt(0)
	v_mov_b64_e32 v[32:33], 0
	v_mov_b64_e32 v[34:35], 0
	v_mov_b64_e32 v[20:21], 0
	v_mov_b64_e32 v[22:23], 0
	v_mov_b64_e32 v[16:17], 0
	v_mov_b64_e32 v[18:19], 0
	v_mov_b64_e32 v[4:5], 0
	v_mov_b64_e32 v[6:7], 0
	v_mov_b64_e32 v[0:1], 0
	v_mov_b64_e32 v[2:3], 0

.LBB0_2051:
	s_ashr_i32 s9, s8, 31
	s_lshl_b64 s[12:13], s[8:9], 18
	v_readlane_b32 s14, v254, 44
	v_readlane_b32 s15, v254, 45
	s_add_u32 s12, s14, s12
	s_addc_u32 s13, s15, s13
	s_and_b64 s[14:15], s[10:11], exec
	s_cselect_b32 s9, s13, s25
	s_cselect_b32 s46, s12, s24
	s_ashr_i32 s7, s6, 31
	s_lshl_b64 s[14:15], s[6:7], 18
	s_add_u32 s14, s18, s14
	s_addc_u32 s15, s19, s15
	s_and_b64 s[28:29], s[10:11], exec
	s_cselect_b32 s7, s15, s27
	s_cselect_b32 s47, s14, s26
	s_add_u32 s24, s24, 0x20080
	s_addc_u32 s25, s25, 0
	s_add_u32 s48, s26, 0x100
	v_mov_b32_e32 v48, 0
	s_addc_u32 s49, s27, 0
	s_mov_b32 s50, -2
	v_mov_b32_e32 v49, v48
	v_mov_b64_e32 v[50:51], 0
	v_mov_b64_e32 v[52:53], 0
	v_mov_b64_e32 v[54:55], 0
	v_mov_b64_e32 v[72:73], 0
	v_mov_b64_e32 v[74:75], 0
	v_mov_b64_e32 v[76:77], 0
	v_mov_b64_e32 v[78:79], 0
	v_mov_b64_e32 v[88:89], 0
	v_mov_b64_e32 v[90:91], 0
	v_mov_b64_e32 v[92:93], 0
	v_mov_b64_e32 v[94:95], 0
	v_mov_b64_e32 v[108:109], 0
	v_mov_b64_e32 v[110:111], 0
	v_mov_b64_e32 v[116:117], 0
	v_mov_b64_e32 v[118:119], 0
	v_mov_b64_e32 v[124:125], 0
	v_mov_b64_e32 v[126:127], 0
	v_mov_b64_e32 v[132:133], 0
	v_mov_b64_e32 v[134:135], 0
	v_mov_b64_e32 v[140:141], 0
	v_mov_b64_e32 v[142:143], 0
	v_mov_b64_e32 v[148:149], 0
	v_mov_b64_e32 v[150:151], 0
	v_mov_b64_e32 v[104:105], 0
	v_mov_b64_e32 v[106:107], 0
	v_mov_b64_e32 v[112:113], 0
	v_mov_b64_e32 v[114:115], 0
	v_mov_b64_e32 v[120:121], 0
	v_mov_b64_e32 v[122:123], 0
	v_mov_b64_e32 v[128:129], 0
	v_mov_b64_e32 v[130:131], 0
	v_mov_b64_e32 v[136:137], 0
	v_mov_b64_e32 v[138:139], 0
	v_mov_b64_e32 v[144:145], 0
	v_mov_b64_e32 v[146:147], 0
	v_mov_b64_e32 v[152:153], 0
	v_mov_b64_e32 v[154:155], 0
	v_mov_b64_e32 v[156:157], 0
	v_mov_b64_e32 v[158:159], 0
	v_mov_b64_e32 v[60:61], 0
	v_mov_b64_e32 v[62:63], 0
	v_mov_b64_e32 v[56:57], 0
	v_mov_b64_e32 v[58:59], 0
	v_mov_b64_e32 v[36:37], 0
	v_mov_b64_e32 v[38:39], 0
	v_mov_b64_e32 v[32:33], 0
	v_mov_b64_e32 v[34:35], 0
	v_mov_b64_e32 v[100:101], 0
	v_mov_b64_e32 v[102:103], 0
	v_mov_b64_e32 v[96:97], 0
	v_mov_b64_e32 v[98:99], 0
	v_mov_b64_e32 v[84:85], 0
	v_mov_b64_e32 v[86:87], 0
	v_mov_b64_e32 v[80:81], 0
	v_mov_b64_e32 v[82:83], 0
	v_mov_b64_e32 v[68:69], 0
	v_mov_b64_e32 v[70:71], 0
	v_mov_b64_e32 v[64:65], 0
	v_mov_b64_e32 v[66:67], 0
	v_mov_b64_e32 v[44:45], 0
	v_mov_b64_e32 v[46:47], 0
	v_mov_b64_e32 v[40:41], 0
	v_mov_b64_e32 v[42:43], 0

.LBB0_2379:
	s_ashr_i32 s37, s36, 31
	s_lshl_b64 s[42:43], s[36:37], 18
	v_readlane_b32 s1, v254, 48
	s_add_u32 s42, s1, s42
	v_readlane_b32 s1, v254, 49
	s_addc_u32 s43, s1, s43
	s_and_b64 s[44:45], s[40:41], exec
	s_cselect_b32 s1, s43, s3
	s_cselect_b32 s5, s42, s2
	s_ashr_i32 s39, s38, 31
	s_lshl_b64 s[44:45], s[38:39], 18
	s_add_u32 s44, s35, s44
	s_addc_u32 s45, s54, s45
	s_and_b64 s[46:47], s[40:41], exec
	s_cselect_b32 s33, s45, s7
	s_cselect_b32 s37, s44, s6
	s_add_u32 s2, s2, 0x20080
	s_addc_u32 s3, s3, 0
	s_add_u32 s39, s6, 0x100
	v_mov_b32_e32 v64, 0
	s_addc_u32 s48, s7, 0
	s_mov_b32 s49, -2
	v_mov_b32_e32 v65, v64
	v_mov_b64_e32 v[66:67], 0
	v_mov_b64_e32 v[68:69], 0
	v_mov_b64_e32 v[70:71], 0
	v_mov_b64_e32 v[80:81], 0
	v_mov_b64_e32 v[82:83], 0
	v_mov_b64_e32 v[84:85], 0
	v_mov_b64_e32 v[86:87], 0
	v_mov_b64_e32 v[96:97], 0
	v_mov_b64_e32 v[98:99], 0
	v_mov_b64_e32 v[100:101], 0
	v_mov_b64_e32 v[102:103], 0
	v_mov_b64_e32 v[112:113], 0
	v_mov_b64_e32 v[114:115], 0
	v_mov_b64_e32 v[116:117], 0
	v_mov_b64_e32 v[118:119], 0
	v_mov_b64_e32 v[128:129], 0
	v_mov_b64_e32 v[130:131], 0
	v_mov_b64_e32 v[132:133], 0
	v_mov_b64_e32 v[134:135], 0
	v_mov_b64_e32 v[144:145], 0
	v_mov_b64_e32 v[146:147], 0
	v_mov_b64_e32 v[148:149], 0
	v_mov_b64_e32 v[150:151], 0
	v_mov_b64_e32 v[104:105], 0
	v_mov_b64_e32 v[106:107], 0
	v_mov_b64_e32 v[108:109], 0
	v_mov_b64_e32 v[110:111], 0
	v_mov_b64_e32 v[120:121], 0
	v_mov_b64_e32 v[122:123], 0
	v_mov_b64_e32 v[124:125], 0
	v_mov_b64_e32 v[126:127], 0
	v_mov_b64_e32 v[136:137], 0
	v_mov_b64_e32 v[138:139], 0
	v_mov_b64_e32 v[140:141], 0
	v_mov_b64_e32 v[142:143], 0
	v_mov_b64_e32 v[152:153], 0
	v_mov_b64_e32 v[154:155], 0
	v_mov_b64_e32 v[156:157], 0
	v_mov_b64_e32 v[158:159], 0
	v_mov_b64_e32 v[56:57], 0
	v_mov_b64_e32 v[58:59], 0
	v_mov_b64_e32 v[48:49], 0
	v_mov_b64_e32 v[50:51], 0
	v_mov_b64_e32 v[40:41], 0
	v_mov_b64_e32 v[42:43], 0
	s_waitcnt vmcnt(0)
	v_mov_b64_e32 v[32:33], 0
	v_mov_b64_e32 v[34:35], 0
	v_mov_b64_e32 v[92:93], 0
	v_mov_b64_e32 v[94:95], 0
	v_mov_b64_e32 v[88:89], 0
	v_mov_b64_e32 v[90:91], 0
	v_mov_b64_e32 v[76:77], 0
	v_mov_b64_e32 v[78:79], 0
	v_mov_b64_e32 v[72:73], 0
	v_mov_b64_e32 v[74:75], 0
	v_mov_b64_e32 v[60:61], 0
	v_mov_b64_e32 v[62:63], 0
	v_mov_b64_e32 v[52:53], 0
	v_mov_b64_e32 v[54:55], 0
	v_mov_b64_e32 v[44:45], 0
	v_mov_b64_e32 v[46:47], 0
	v_mov_b64_e32 v[36:37], 0
	v_mov_b64_e32 v[38:39], 0

.LBB0_2570:
	s_ashr_i32 s35, s34, 31
	s_lshl_b64 s[36:37], s[34:35], 18
	s_add_u32 s36, s10, s36
	v_lshlrev_b64 v[2:3], 20, v[166:167]
	s_addc_u32 s37, s11, s37
	v_lshl_add_u64 v[168:169], s[36:37], 0, v[2:3]
	v_cndmask_b32_e64 v167, v1, v169, s[4:5]
	v_cndmask_b32_e64 v220, v0, v168, s[4:5]
	v_mov_b32_e32 v173, v161
	v_mov_b32_e32 v175, v161
	s_mov_b64 s[4:5], 0x100
	v_mov_b32_e32 v64, 0
	v_lshl_add_u64 v[176:177], s[24:25], 0, v[174:175]
	v_lshl_add_u64 v[178:179], s[24:25], 0, v[172:173]
	v_lshl_add_u64 v[180:181], v[0:1], 0, s[4:5]
	s_mov_b32 s35, -2
	s_mov_b64 s[4:5], 0
	v_mov_b32_e32 v65, v64
	v_mov_b64_e32 v[66:67], 0
	v_mov_b64_e32 v[68:69], 0
	v_mov_b64_e32 v[70:71], 0
	v_mov_b64_e32 v[80:81], 0
	v_mov_b64_e32 v[82:83], 0
	v_mov_b64_e32 v[84:85], 0
	v_mov_b64_e32 v[86:87], 0
	v_mov_b64_e32 v[96:97], 0
	v_mov_b64_e32 v[98:99], 0
	v_mov_b64_e32 v[100:101], 0
	v_mov_b64_e32 v[102:103], 0
	v_mov_b64_e32 v[112:113], 0
	v_mov_b64_e32 v[114:115], 0
	v_mov_b64_e32 v[116:117], 0
	v_mov_b64_e32 v[118:119], 0
	v_mov_b64_e32 v[128:129], 0
	v_mov_b64_e32 v[130:131], 0
	v_mov_b64_e32 v[132:133], 0
	v_mov_b64_e32 v[134:135], 0
	v_mov_b64_e32 v[144:145], 0
	v_mov_b64_e32 v[146:147], 0
	v_mov_b64_e32 v[148:149], 0
	v_mov_b64_e32 v[150:151], 0
	v_mov_b64_e32 v[104:105], 0
	v_mov_b64_e32 v[106:107], 0
	v_mov_b64_e32 v[108:109], 0
	v_mov_b64_e32 v[110:111], 0
	v_mov_b64_e32 v[120:121], 0
	v_mov_b64_e32 v[122:123], 0
	v_mov_b64_e32 v[124:125], 0
	v_mov_b64_e32 v[126:127], 0
	v_mov_b64_e32 v[136:137], 0
	v_mov_b64_e32 v[138:139], 0
	v_mov_b64_e32 v[140:141], 0
	v_mov_b64_e32 v[142:143], 0
	v_mov_b64_e32 v[152:153], 0
	v_mov_b64_e32 v[154:155], 0
	v_mov_b64_e32 v[156:157], 0
	v_mov_b64_e32 v[158:159], 0
	v_mov_b64_e32 v[52:53], 0
	v_mov_b64_e32 v[54:55], 0
	v_mov_b64_e32 v[48:49], 0
	v_mov_b64_e32 v[50:51], 0
	v_mov_b64_e32 v[36:37], 0
	v_mov_b64_e32 v[38:39], 0
	v_mov_b64_e32 v[32:33], 0
	v_mov_b64_e32 v[34:35], 0
	v_mov_b64_e32 v[92:93], 0
	v_mov_b64_e32 v[94:95], 0
	v_mov_b64_e32 v[88:89], 0
	v_mov_b64_e32 v[90:91], 0
	v_mov_b64_e32 v[76:77], 0
	v_mov_b64_e32 v[78:79], 0
	v_mov_b64_e32 v[72:73], 0
	v_mov_b64_e32 v[74:75], 0
	v_mov_b64_e32 v[60:61], 0
	v_mov_b64_e32 v[62:63], 0
	v_mov_b64_e32 v[56:57], 0
	v_mov_b64_e32 v[58:59], 0
	v_mov_b64_e32 v[44:45], 0
	v_mov_b64_e32 v[46:47], 0
	v_mov_b64_e32 v[40:41], 0
	v_mov_b64_e32 v[42:43], 0

.LBB0_2587:
	s_ashr_i32 s13, s12, 31
	s_lshl_b64 s[16:17], s[12:13], 17
	s_add_u32 s16, s33, s16
	s_addc_u32 s17, s48, s17
	s_and_b64 s[24:25], s[2:3], exec
	s_cselect_b32 s13, s17, s29
	s_cselect_b32 s61, s16, s28
	s_ashr_i32 s15, s14, 31
	s_lshl_b64 s[24:25], s[14:15], 17
	s_add_u32 s24, s49, s24
	s_addc_u32 s25, s50, s25
	s_and_b64 s[30:31], s[2:3], exec
	v_mov_b32_e32 v0, 0
	s_cselect_b32 s15, s25, s27
	s_cselect_b32 s62, s24, s26
	s_mov_b64 s[36:37], 0
	s_mov_b64 s[30:31], -1
	s_mov_b64 s[34:35], 0
	v_mov_b32_e32 v1, v0
	v_mov_b64_e32 v[2:3], 0
	v_mov_b64_e32 v[4:5], 0
	v_mov_b64_e32 v[6:7], 0
	v_mov_b64_e32 v[32:33], 0
	v_mov_b64_e32 v[34:35], 0
	v_mov_b64_e32 v[44:45], 0
	v_mov_b64_e32 v[46:47], 0
	v_mov_b64_e32 v[48:49], 0
	v_mov_b64_e32 v[50:51], 0
	v_mov_b64_e32 v[52:53], 0
	v_mov_b64_e32 v[54:55], 0
	v_mov_b64_e32 v[72:73], 0
	v_mov_b64_e32 v[74:75], 0
	v_mov_b64_e32 v[80:81], 0
	v_mov_b64_e32 v[82:83], 0
	v_mov_b64_e32 v[88:89], 0
	v_mov_b64_e32 v[90:91], 0
	v_mov_b64_e32 v[96:97], 0
	v_mov_b64_e32 v[98:99], 0
	v_mov_b64_e32 v[104:105], 0
	v_mov_b64_e32 v[106:107], 0
	v_mov_b64_e32 v[112:113], 0
	v_mov_b64_e32 v[114:115], 0
	v_mov_b64_e32 v[76:77], 0
	v_mov_b64_e32 v[78:79], 0
	v_mov_b64_e32 v[84:85], 0
	v_mov_b64_e32 v[86:87], 0
	v_mov_b64_e32 v[92:93], 0
	v_mov_b64_e32 v[94:95], 0
	v_mov_b64_e32 v[100:101], 0
	v_mov_b64_e32 v[102:103], 0
	v_mov_b64_e32 v[108:109], 0
	v_mov_b64_e32 v[110:111], 0
	v_mov_b64_e32 v[116:117], 0
	v_mov_b64_e32 v[118:119], 0
	v_mov_b64_e32 v[120:121], 0
	v_mov_b64_e32 v[122:123], 0
	v_mov_b64_e32 v[124:125], 0
	v_mov_b64_e32 v[126:127], 0
	v_mov_b64_e32 v[28:29], 0
	v_mov_b64_e32 v[30:31], 0
	v_mov_b64_e32 v[24:25], 0
	v_mov_b64_e32 v[26:27], 0
	v_mov_b64_e32 v[12:13], 0
	v_mov_b64_e32 v[14:15], 0
	v_mov_b64_e32 v[8:9], 0
	v_mov_b64_e32 v[10:11], 0
	v_mov_b64_e32 v[68:69], 0
	v_mov_b64_e32 v[70:71], 0
	v_mov_b64_e32 v[64:65], 0
	v_mov_b64_e32 v[66:67], 0
	v_mov_b64_e32 v[60:61], 0
	v_mov_b64_e32 v[62:63], 0
	v_mov_b64_e32 v[56:57], 0
	v_mov_b64_e32 v[58:59], 0
	v_mov_b64_e32 v[40:41], 0
	v_mov_b64_e32 v[42:43], 0
	v_mov_b64_e32 v[36:37], 0
	v_mov_b64_e32 v[38:39], 0
	v_mov_b64_e32 v[20:21], 0
	v_mov_b64_e32 v[22:23], 0
	v_mov_b64_e32 v[16:17], 0
	v_mov_b64_e32 v[18:19], 0

.LBB0_2668:
	s_ashr_i32 s27, s26, 31
	s_lshl_b64 s[28:29], s[26:27], 17
	v_readlane_b32 s30, v254, 46
	v_readlane_b32 s31, v254, 47
	s_add_u32 s28, s30, s28
	s_addc_u32 s29, s31, s29
	s_and_b64 s[30:31], s[4:5], exec
	s_cselect_b32 s27, s29, s25
	s_cselect_b32 s78, s28, s24
	s_ashr_i32 s15, s14, 31
	s_lshl_b64 s[30:31], s[14:15], 17
	v_ashrrev_i32_e32 v171, 31, v170
	s_add_u32 s30, s17, s30
	v_lshlrev_b64 v[0:1], 19, v[170:171]
	s_addc_u32 s31, s42, s31
	v_lshl_add_u64 v[172:173], s[30:31], 0, v[0:1]
	v_mov_b32_e32 v48, 0
	v_cndmask_b32_e64 v171, v169, v173, s[4:5]
	v_cndmask_b32_e64 v205, v168, v172, s[4:5]
	s_mov_b64 s[36:37], 0
	s_mov_b64 s[30:31], -1
	s_mov_b64 s[34:35], 0
	v_mov_b32_e32 v49, v48
	v_mov_b64_e32 v[50:51], 0
	v_mov_b64_e32 v[60:61], 0
	v_mov_b64_e32 v[62:63], 0
	v_mov_b64_e32 v[76:77], 0
	v_mov_b64_e32 v[78:79], 0
	v_mov_b64_e32 v[84:85], 0
	v_mov_b64_e32 v[86:87], 0
	v_mov_b64_e32 v[88:89], 0
	v_mov_b64_e32 v[90:91], 0
	v_mov_b64_e32 v[96:97], 0
	v_mov_b64_e32 v[98:99], 0
	v_mov_b64_e32 v[112:113], 0
	v_mov_b64_e32 v[114:115], 0
	v_mov_b64_e32 v[116:117], 0
	v_mov_b64_e32 v[118:119], 0
	v_mov_b64_e32 v[128:129], 0
	v_mov_b64_e32 v[130:131], 0
	v_mov_b64_e32 v[132:133], 0
	v_mov_b64_e32 v[134:135], 0
	v_mov_b64_e32 v[144:145], 0
	v_mov_b64_e32 v[146:147], 0
	v_mov_b64_e32 v[148:149], 0
	v_mov_b64_e32 v[150:151], 0
	v_mov_b64_e32 v[104:105], 0
	v_mov_b64_e32 v[106:107], 0
	v_mov_b64_e32 v[108:109], 0
	v_mov_b64_e32 v[110:111], 0
	v_mov_b64_e32 v[120:121], 0
	v_mov_b64_e32 v[122:123], 0
	v_mov_b64_e32 v[124:125], 0
	v_mov_b64_e32 v[126:127], 0
	v_mov_b64_e32 v[136:137], 0
	v_mov_b64_e32 v[138:139], 0
	v_mov_b64_e32 v[140:141], 0
	v_mov_b64_e32 v[142:143], 0
	v_mov_b64_e32 v[152:153], 0
	v_mov_b64_e32 v[154:155], 0
	v_mov_b64_e32 v[156:157], 0
	v_mov_b64_e32 v[158:159], 0
	v_mov_b64_e32 v[68:69], 0
	v_mov_b64_e32 v[70:71], 0
	v_mov_b64_e32 v[56:57], 0
	v_mov_b64_e32 v[58:59], 0
	v_mov_b64_e32 v[44:45], 0
	v_mov_b64_e32 v[46:47], 0
	v_mov_b64_e32 v[36:37], 0
	v_mov_b64_e32 v[38:39], 0
	v_mov_b64_e32 v[100:101], 0
	v_mov_b64_e32 v[102:103], 0
	v_mov_b64_e32 v[92:93], 0
	v_mov_b64_e32 v[94:95], 0
	v_mov_b64_e32 v[80:81], 0
	v_mov_b64_e32 v[82:83], 0
	v_mov_b64_e32 v[72:73], 0
	v_mov_b64_e32 v[74:75], 0
	v_mov_b64_e32 v[64:65], 0
	v_mov_b64_e32 v[66:67], 0
	v_mov_b64_e32 v[52:53], 0
	v_mov_b64_e32 v[54:55], 0
	v_mov_b64_e32 v[40:41], 0
	v_mov_b64_e32 v[42:43], 0
	v_mov_b64_e32 v[32:33], 0
	v_mov_b64_e32 v[34:35], 0

.LBB0_2837:
	s_ashr_i32 s11, s10, 31
	s_lshl_b64 s[12:13], s[10:11], 17
	s_add_u32 s12, s45, s12
	s_addc_u32 s13, s46, s13
	s_and_b64 s[14:15], s[2:3], exec
	s_cselect_b32 s11, s13, s25
	s_cselect_b32 s59, s12, s24
	s_ashr_i32 s9, s8, 31
	s_lshl_b64 s[14:15], s[8:9], 17
	s_add_u32 s14, s47, s14
	s_addc_u32 s15, s48, s15
	s_and_b64 s[26:27], s[2:3], exec
	v_mov_b32_e32 v0, 0
	s_cselect_b32 s9, s15, s23
	s_cselect_b32 s60, s14, s22
	s_mov_b64 s[30:31], 0
	s_mov_b64 s[26:27], -1
	s_mov_b64 s[28:29], 0
	v_mov_b32_e32 v1, v0
	v_mov_b64_e32 v[2:3], 0
	v_mov_b64_e32 v[4:5], 0
	v_mov_b64_e32 v[6:7], 0
	v_mov_b64_e32 v[32:33], 0
	v_mov_b64_e32 v[34:35], 0
	v_mov_b64_e32 v[44:45], 0
	v_mov_b64_e32 v[46:47], 0
	v_mov_b64_e32 v[48:49], 0
	v_mov_b64_e32 v[50:51], 0
	v_mov_b64_e32 v[52:53], 0
	v_mov_b64_e32 v[54:55], 0
	v_mov_b64_e32 v[72:73], 0
	v_mov_b64_e32 v[74:75], 0
	v_mov_b64_e32 v[80:81], 0
	v_mov_b64_e32 v[82:83], 0
	v_mov_b64_e32 v[88:89], 0
	v_mov_b64_e32 v[90:91], 0
	v_mov_b64_e32 v[96:97], 0
	v_mov_b64_e32 v[98:99], 0
	v_mov_b64_e32 v[104:105], 0
	v_mov_b64_e32 v[106:107], 0
	v_mov_b64_e32 v[112:113], 0
	v_mov_b64_e32 v[114:115], 0
	v_mov_b64_e32 v[76:77], 0
	v_mov_b64_e32 v[78:79], 0
	v_mov_b64_e32 v[84:85], 0
	v_mov_b64_e32 v[86:87], 0
	v_mov_b64_e32 v[92:93], 0
	v_mov_b64_e32 v[94:95], 0
	v_mov_b64_e32 v[100:101], 0
	v_mov_b64_e32 v[102:103], 0
	v_mov_b64_e32 v[108:109], 0
	v_mov_b64_e32 v[110:111], 0
	v_mov_b64_e32 v[116:117], 0
	v_mov_b64_e32 v[118:119], 0
	v_mov_b64_e32 v[120:121], 0
	v_mov_b64_e32 v[122:123], 0
	v_mov_b64_e32 v[124:125], 0
	v_mov_b64_e32 v[126:127], 0
	v_mov_b64_e32 v[28:29], 0
	v_mov_b64_e32 v[30:31], 0
	v_mov_b64_e32 v[24:25], 0
	v_mov_b64_e32 v[26:27], 0
	v_mov_b64_e32 v[12:13], 0
	v_mov_b64_e32 v[14:15], 0
	v_mov_b64_e32 v[8:9], 0
	v_mov_b64_e32 v[10:11], 0
	v_mov_b64_e32 v[68:69], 0
	v_mov_b64_e32 v[70:71], 0
	v_mov_b64_e32 v[64:65], 0
	v_mov_b64_e32 v[66:67], 0
	v_mov_b64_e32 v[60:61], 0
	v_mov_b64_e32 v[62:63], 0
	v_mov_b64_e32 v[56:57], 0
	v_mov_b64_e32 v[58:59], 0
	v_mov_b64_e32 v[40:41], 0
	v_mov_b64_e32 v[42:43], 0
	v_mov_b64_e32 v[36:37], 0
	v_mov_b64_e32 v[38:39], 0
	v_mov_b64_e32 v[20:21], 0
	v_mov_b64_e32 v[22:23], 0
	v_mov_b64_e32 v[16:17], 0
	v_mov_b64_e32 v[18:19], 0

.LBB0_2858:
	s_ashr_i32 s15, s14, 31
	s_lshl_b64 s[22:23], s[14:15], 19
	s_add_u32 s22, s18, s22
	s_addc_u32 s23, s19, s23
	s_and_b64 s[24:25], s[16:17], exec
	s_cselect_b32 s15, s23, s29
	s_cselect_b32 s50, s22, s28
	s_ashr_i32 s13, s12, 31
	s_lshl_b64 s[24:25], s[12:13], 19
	s_add_u32 s24, s33, s24
	s_addc_u32 s25, s36, s25
	s_and_b64 s[34:35], s[16:17], exec
	s_cselect_b32 s13, s25, s31
	s_cselect_b32 s51, s24, s30
	s_add_u32 s28, s28, 0x40080
	s_addc_u32 s29, s29, 0
	s_add_u32 s52, s30, 0x100
	v_mov_b32_e32 v36, 0
	s_addc_u32 s53, s31, 0
	s_mov_b32 s54, -2
	v_mov_b32_e32 v37, v36
	v_mov_b64_e32 v[38:39], 0
	v_mov_b64_e32 v[44:45], 0
	v_mov_b64_e32 v[46:47], 0
	v_mov_b64_e32 v[52:53], 0
	v_mov_b64_e32 v[54:55], 0
	v_mov_b64_e32 v[60:61], 0
	v_mov_b64_e32 v[62:63], 0
	v_mov_b64_e32 v[64:65], 0
	v_mov_b64_e32 v[66:67], 0
	v_mov_b64_e32 v[68:69], 0
	v_mov_b64_e32 v[70:71], 0
	v_mov_b64_e32 v[80:81], 0
	v_mov_b64_e32 v[82:83], 0
	v_mov_b64_e32 v[84:85], 0
	v_mov_b64_e32 v[86:87], 0
	v_mov_b64_e32 v[96:97], 0
	v_mov_b64_e32 v[98:99], 0
	v_mov_b64_e32 v[100:101], 0
	v_mov_b64_e32 v[102:103], 0
	v_mov_b64_e32 v[112:113], 0
	v_mov_b64_e32 v[114:115], 0
	v_mov_b64_e32 v[116:117], 0
	v_mov_b64_e32 v[118:119], 0
	v_mov_b64_e32 v[72:73], 0
	v_mov_b64_e32 v[74:75], 0
	v_mov_b64_e32 v[76:77], 0
	v_mov_b64_e32 v[78:79], 0
	v_mov_b64_e32 v[88:89], 0
	v_mov_b64_e32 v[90:91], 0
	v_mov_b64_e32 v[92:93], 0
	v_mov_b64_e32 v[94:95], 0
	v_mov_b64_e32 v[104:105], 0
	v_mov_b64_e32 v[106:107], 0
	v_mov_b64_e32 v[108:109], 0
	v_mov_b64_e32 v[110:111], 0
	v_mov_b64_e32 v[128:129], 0
	v_mov_b64_e32 v[130:131], 0
	v_mov_b64_e32 v[120:121], 0
	v_mov_b64_e32 v[122:123], 0
	v_mov_b64_e32 v[28:29], 0
	v_mov_b64_e32 v[30:31], 0
	v_mov_b64_e32 v[24:25], 0
	v_mov_b64_e32 v[26:27], 0
	v_mov_b64_e32 v[12:13], 0
	v_mov_b64_e32 v[14:15], 0
	v_mov_b64_e32 v[8:9], 0
	v_mov_b64_e32 v[10:11], 0
	v_mov_b64_e32 v[56:57], 0
	v_mov_b64_e32 v[58:59], 0
	v_mov_b64_e32 v[48:49], 0
	v_mov_b64_e32 v[50:51], 0
	v_mov_b64_e32 v[40:41], 0
	v_mov_b64_e32 v[42:43], 0
	s_waitcnt vmcnt(0)
	v_mov_b64_e32 v[32:33], 0
	v_mov_b64_e32 v[34:35], 0
	v_mov_b64_e32 v[20:21], 0
	v_mov_b64_e32 v[22:23], 0
	v_mov_b64_e32 v[16:17], 0
	v_mov_b64_e32 v[18:19], 0
	v_mov_b64_e32 v[4:5], 0
	v_mov_b64_e32 v[6:7], 0
	v_mov_b64_e32 v[0:1], 0
	v_mov_b64_e32 v[2:3], 0

.LBB0_2931:
	s_ashr_i32 s15, s14, 31
	s_lshl_b64 s[18:19], s[14:15], 18
	v_readlane_b32 s20, v254, 44
	v_readlane_b32 s21, v254, 45
	s_add_u32 s18, s20, s18
	s_addc_u32 s19, s21, s19
	s_and_b64 s[20:21], s[16:17], exec
	s_cselect_b32 s15, s19, s23
	s_cselect_b32 s54, s18, s22
	s_ashr_i32 s13, s12, 31
	s_lshl_b64 s[20:21], s[12:13], 18
	s_add_u32 s20, s28, s20
	s_addc_u32 s21, s29, s21
	s_and_b64 s[26:27], s[16:17], exec
	s_cselect_b32 s13, s21, s25
	s_cselect_b32 s55, s20, s24
	s_add_u32 s22, s22, 0x20080
	s_addc_u32 s23, s23, 0
	s_add_u32 s56, s24, 0x100
	v_mov_b32_e32 v64, 0
	s_addc_u32 s57, s25, 0
	s_mov_b32 s58, -2
	v_mov_b32_e32 v65, v64
	v_mov_b64_e32 v[66:67], 0
	v_mov_b64_e32 v[116:117], 0
	v_mov_b64_e32 v[118:119], 0
	v_mov_b64_e32 v[84:85], 0
	v_mov_b64_e32 v[86:87], 0
	v_mov_b64_e32 v[128:129], 0
	v_mov_b64_e32 v[130:131], 0
	v_mov_b64_e32 v[32:33], 0
	v_mov_b64_e32 v[34:35], 0
	v_mov_b64_e32 v[48:49], 0
	v_mov_b64_e32 v[50:51], 0
	v_mov_b64_e32 v[36:37], 0
	v_mov_b64_e32 v[38:39], 0
	v_mov_b64_e32 v[52:53], 0
	v_mov_b64_e32 v[54:55], 0
	v_mov_b64_e32 v[40:41], 0
	v_mov_b64_e32 v[42:43], 0
	v_mov_b64_e32 v[56:57], 0
	v_mov_b64_e32 v[58:59], 0
	v_mov_b64_e32 v[44:45], 0
	v_mov_b64_e32 v[46:47], 0
	v_mov_b64_e32 v[72:73], 0
	v_mov_b64_e32 v[74:75], 0
	v_mov_b64_e32 v[96:97], 0
	v_mov_b64_e32 v[98:99], 0
	v_mov_b64_e32 v[136:137], 0
	v_mov_b64_e32 v[138:139], 0
	v_mov_b64_e32 v[108:109], 0
	v_mov_b64_e32 v[110:111], 0
	v_mov_b64_e32 v[140:141], 0
	v_mov_b64_e32 v[142:143], 0
	v_mov_b64_e32 v[112:113], 0
	v_mov_b64_e32 v[114:115], 0
	v_mov_b64_e32 v[144:145], 0
	v_mov_b64_e32 v[146:147], 0
	v_mov_b64_e32 v[124:125], 0
	v_mov_b64_e32 v[126:127], 0
	v_mov_b64_e32 v[156:157], 0
	v_mov_b64_e32 v[158:159], 0
	v_mov_b64_e32 v[148:149], 0
	v_mov_b64_e32 v[150:151], 0
	v_mov_b64_e32 v[120:121], 0
	v_mov_b64_e32 v[122:123], 0
	v_mov_b64_e32 v[152:153], 0
	v_mov_b64_e32 v[154:155], 0
	v_mov_b64_e32 v[132:133], 0
	v_mov_b64_e32 v[134:135], 0
	v_mov_b64_e32 v[88:89], 0
	v_mov_b64_e32 v[90:91], 0
	v_mov_b64_e32 v[60:61], 0
	v_mov_b64_e32 v[62:63], 0
	v_mov_b64_e32 v[92:93], 0
	v_mov_b64_e32 v[94:95], 0
	v_mov_b64_e32 v[68:69], 0
	v_mov_b64_e32 v[70:71], 0
	v_mov_b64_e32 v[100:101], 0
	v_mov_b64_e32 v[102:103], 0
	v_mov_b64_e32 v[76:77], 0
	v_mov_b64_e32 v[78:79], 0
	v_mov_b64_e32 v[104:105], 0
	v_mov_b64_e32 v[106:107], 0
	v_mov_b64_e32 v[80:81], 0
	v_mov_b64_e32 v[82:83], 0

.LBB0_3318:
	s_ashr_i32 s31, s30, 31
	s_lshl_b64 s[34:35], s[30:31], 18
	s_add_u32 s34, s10, s34
	v_lshlrev_b64 v[2:3], 20, v[166:167]
	s_addc_u32 s35, s11, s35
	v_lshl_add_u64 v[168:169], s[34:35], 0, v[2:3]
	v_cndmask_b32_e64 v167, v1, v169, s[4:5]
	v_cndmask_b32_e64 v220, v0, v168, s[4:5]
	v_mov_b32_e32 v173, v161
	v_mov_b32_e32 v175, v161
	s_mov_b64 s[4:5], 0x100
	v_mov_b32_e32 v64, 0
	v_lshl_add_u64 v[176:177], s[22:23], 0, v[174:175]
	v_lshl_add_u64 v[178:179], s[22:23], 0, v[172:173]
	v_lshl_add_u64 v[180:181], v[0:1], 0, s[4:5]
	s_mov_b32 s31, -2
	s_mov_b64 s[4:5], 0
	v_mov_b32_e32 v65, v64
	v_mov_b64_e32 v[66:67], 0
	v_mov_b64_e32 v[68:69], 0
	v_mov_b64_e32 v[70:71], 0
	v_mov_b64_e32 v[80:81], 0
	v_mov_b64_e32 v[82:83], 0
	v_mov_b64_e32 v[84:85], 0
	v_mov_b64_e32 v[86:87], 0
	v_mov_b64_e32 v[96:97], 0
	v_mov_b64_e32 v[98:99], 0
	v_mov_b64_e32 v[100:101], 0
	v_mov_b64_e32 v[102:103], 0
	v_mov_b64_e32 v[112:113], 0
	v_mov_b64_e32 v[114:115], 0
	v_mov_b64_e32 v[116:117], 0
	v_mov_b64_e32 v[118:119], 0
	v_mov_b64_e32 v[128:129], 0
	v_mov_b64_e32 v[130:131], 0
	v_mov_b64_e32 v[132:133], 0
	v_mov_b64_e32 v[134:135], 0
	v_mov_b64_e32 v[144:145], 0
	v_mov_b64_e32 v[146:147], 0
	v_mov_b64_e32 v[148:149], 0
	v_mov_b64_e32 v[150:151], 0
	v_mov_b64_e32 v[104:105], 0
	v_mov_b64_e32 v[106:107], 0
	v_mov_b64_e32 v[108:109], 0
	v_mov_b64_e32 v[110:111], 0
	v_mov_b64_e32 v[120:121], 0
	v_mov_b64_e32 v[122:123], 0
	v_mov_b64_e32 v[124:125], 0
	v_mov_b64_e32 v[126:127], 0
	v_mov_b64_e32 v[136:137], 0
	v_mov_b64_e32 v[138:139], 0
	v_mov_b64_e32 v[140:141], 0
	v_mov_b64_e32 v[142:143], 0
	v_mov_b64_e32 v[152:153], 0
	v_mov_b64_e32 v[154:155], 0
	v_mov_b64_e32 v[156:157], 0
	v_mov_b64_e32 v[158:159], 0
	v_mov_b64_e32 v[52:53], 0
	v_mov_b64_e32 v[54:55], 0
	v_mov_b64_e32 v[48:49], 0
	v_mov_b64_e32 v[50:51], 0
	v_mov_b64_e32 v[36:37], 0
	v_mov_b64_e32 v[38:39], 0
	v_mov_b64_e32 v[32:33], 0
	v_mov_b64_e32 v[34:35], 0
	v_mov_b64_e32 v[92:93], 0
	v_mov_b64_e32 v[94:95], 0
	v_mov_b64_e32 v[88:89], 0
	v_mov_b64_e32 v[90:91], 0
	v_mov_b64_e32 v[76:77], 0
	v_mov_b64_e32 v[78:79], 0
	v_mov_b64_e32 v[72:73], 0
	v_mov_b64_e32 v[74:75], 0
	v_mov_b64_e32 v[60:61], 0
	v_mov_b64_e32 v[62:63], 0
	v_mov_b64_e32 v[56:57], 0
	v_mov_b64_e32 v[58:59], 0
	v_mov_b64_e32 v[44:45], 0
	v_mov_b64_e32 v[46:47], 0
	v_mov_b64_e32 v[40:41], 0
	v_mov_b64_e32 v[42:43], 0

.LBB0_3335:
	s_ashr_i32 s13, s12, 31
	s_lshl_b64 s[16:17], s[12:13], 17
	s_add_u32 s16, s33, s16
	s_addc_u32 s17, s46, s17
	s_and_b64 s[22:23], s[2:3], exec
	s_cselect_b32 s13, s17, s27
	s_cselect_b32 s60, s16, s26
	s_ashr_i32 s15, s14, 31
	s_lshl_b64 s[22:23], s[14:15], 17
	s_add_u32 s22, s47, s22
	s_addc_u32 s23, s48, s23
	s_and_b64 s[28:29], s[2:3], exec
	v_mov_b32_e32 v0, 0
	s_cselect_b32 s15, s23, s25
	s_cselect_b32 s61, s22, s24
	s_mov_b64 s[34:35], 0
	s_mov_b64 s[28:29], -1
	s_mov_b64 s[30:31], 0
	v_mov_b32_e32 v1, v0
	v_mov_b64_e32 v[2:3], 0
	v_mov_b64_e32 v[4:5], 0
	v_mov_b64_e32 v[6:7], 0
	v_mov_b64_e32 v[32:33], 0
	v_mov_b64_e32 v[34:35], 0
	v_mov_b64_e32 v[44:45], 0
	v_mov_b64_e32 v[46:47], 0
	v_mov_b64_e32 v[48:49], 0
	v_mov_b64_e32 v[50:51], 0
	v_mov_b64_e32 v[52:53], 0
	v_mov_b64_e32 v[54:55], 0
	v_mov_b64_e32 v[72:73], 0
	v_mov_b64_e32 v[74:75], 0
	v_mov_b64_e32 v[80:81], 0
	v_mov_b64_e32 v[82:83], 0
	v_mov_b64_e32 v[88:89], 0
	v_mov_b64_e32 v[90:91], 0
	v_mov_b64_e32 v[96:97], 0
	v_mov_b64_e32 v[98:99], 0
	v_mov_b64_e32 v[104:105], 0
	v_mov_b64_e32 v[106:107], 0
	v_mov_b64_e32 v[112:113], 0
	v_mov_b64_e32 v[114:115], 0
	v_mov_b64_e32 v[76:77], 0
	v_mov_b64_e32 v[78:79], 0
	v_mov_b64_e32 v[84:85], 0
	v_mov_b64_e32 v[86:87], 0
	v_mov_b64_e32 v[92:93], 0
	v_mov_b64_e32 v[94:95], 0
	v_mov_b64_e32 v[100:101], 0
	v_mov_b64_e32 v[102:103], 0
	v_mov_b64_e32 v[108:109], 0
	v_mov_b64_e32 v[110:111], 0
	v_mov_b64_e32 v[116:117], 0
	v_mov_b64_e32 v[118:119], 0
	v_mov_b64_e32 v[120:121], 0
	v_mov_b64_e32 v[122:123], 0
	v_mov_b64_e32 v[124:125], 0
	v_mov_b64_e32 v[126:127], 0
	v_mov_b64_e32 v[28:29], 0
	v_mov_b64_e32 v[30:31], 0
	v_mov_b64_e32 v[24:25], 0
	v_mov_b64_e32 v[26:27], 0
	v_mov_b64_e32 v[12:13], 0
	v_mov_b64_e32 v[14:15], 0
	v_mov_b64_e32 v[8:9], 0
	v_mov_b64_e32 v[10:11], 0
	v_mov_b64_e32 v[68:69], 0
	v_mov_b64_e32 v[70:71], 0
	v_mov_b64_e32 v[64:65], 0
	v_mov_b64_e32 v[66:67], 0
	v_mov_b64_e32 v[60:61], 0
	v_mov_b64_e32 v[62:63], 0
	v_mov_b64_e32 v[56:57], 0
	v_mov_b64_e32 v[58:59], 0
	v_mov_b64_e32 v[40:41], 0
	v_mov_b64_e32 v[42:43], 0
	v_mov_b64_e32 v[36:37], 0
	v_mov_b64_e32 v[38:39], 0
	v_mov_b64_e32 v[20:21], 0
	v_mov_b64_e32 v[22:23], 0
	v_mov_b64_e32 v[16:17], 0
	v_mov_b64_e32 v[18:19], 0

.LBB0_3416:
	s_ashr_i32 s25, s24, 31
	s_lshl_b64 s[26:27], s[24:25], 17
	v_readlane_b32 s28, v254, 46
	v_readlane_b32 s29, v254, 47
	s_add_u32 s26, s28, s26
	s_addc_u32 s27, s29, s27
	s_and_b64 s[28:29], s[4:5], exec
	s_cselect_b32 s25, s27, s23
	s_cselect_b32 s74, s26, s22
	s_ashr_i32 s15, s14, 31
	s_lshl_b64 s[28:29], s[14:15], 17
	v_ashrrev_i32_e32 v171, 31, v170
	s_add_u32 s28, s17, s28
	v_lshlrev_b64 v[0:1], 19, v[170:171]
	s_addc_u32 s29, s40, s29
	v_lshl_add_u64 v[172:173], s[28:29], 0, v[0:1]
	v_mov_b32_e32 v48, 0
	v_cndmask_b32_e64 v171, v169, v173, s[4:5]
	v_cndmask_b32_e64 v205, v168, v172, s[4:5]
	s_mov_b64 s[34:35], 0
	s_mov_b64 s[28:29], -1
	s_mov_b64 s[30:31], 0
	v_mov_b32_e32 v49, v48
	v_mov_b64_e32 v[50:51], 0
	v_mov_b64_e32 v[60:61], 0
	v_mov_b64_e32 v[62:63], 0
	v_mov_b64_e32 v[76:77], 0
	v_mov_b64_e32 v[78:79], 0
	v_mov_b64_e32 v[84:85], 0
	v_mov_b64_e32 v[86:87], 0
	v_mov_b64_e32 v[88:89], 0
	v_mov_b64_e32 v[90:91], 0
	v_mov_b64_e32 v[92:93], 0
	v_mov_b64_e32 v[94:95], 0
	v_mov_b64_e32 v[112:113], 0
	v_mov_b64_e32 v[114:115], 0
	v_mov_b64_e32 v[116:117], 0
	v_mov_b64_e32 v[118:119], 0
	v_mov_b64_e32 v[128:129], 0
	v_mov_b64_e32 v[130:131], 0
	v_mov_b64_e32 v[132:133], 0
	v_mov_b64_e32 v[134:135], 0
	v_mov_b64_e32 v[144:145], 0
	v_mov_b64_e32 v[146:147], 0
	v_mov_b64_e32 v[148:149], 0
	v_mov_b64_e32 v[150:151], 0
	v_mov_b64_e32 v[104:105], 0
	v_mov_b64_e32 v[106:107], 0
	v_mov_b64_e32 v[108:109], 0
	v_mov_b64_e32 v[110:111], 0
	v_mov_b64_e32 v[120:121], 0
	v_mov_b64_e32 v[122:123], 0
	v_mov_b64_e32 v[124:125], 0
	v_mov_b64_e32 v[126:127], 0
	v_mov_b64_e32 v[136:137], 0
	v_mov_b64_e32 v[138:139], 0
	v_mov_b64_e32 v[140:141], 0
	v_mov_b64_e32 v[142:143], 0
	v_mov_b64_e32 v[152:153], 0
	v_mov_b64_e32 v[154:155], 0
	v_mov_b64_e32 v[156:157], 0
	v_mov_b64_e32 v[158:159], 0
	v_mov_b64_e32 v[68:69], 0
	v_mov_b64_e32 v[70:71], 0
	v_mov_b64_e32 v[56:57], 0
	v_mov_b64_e32 v[58:59], 0
	v_mov_b64_e32 v[44:45], 0
	v_mov_b64_e32 v[46:47], 0
	v_mov_b64_e32 v[36:37], 0
	v_mov_b64_e32 v[38:39], 0
	v_mov_b64_e32 v[100:101], 0
	v_mov_b64_e32 v[102:103], 0
	v_mov_b64_e32 v[96:97], 0
	v_mov_b64_e32 v[98:99], 0
	v_mov_b64_e32 v[80:81], 0
	v_mov_b64_e32 v[82:83], 0
	v_mov_b64_e32 v[72:73], 0
	v_mov_b64_e32 v[74:75], 0
	v_mov_b64_e32 v[64:65], 0
	v_mov_b64_e32 v[66:67], 0
	v_mov_b64_e32 v[52:53], 0
	v_mov_b64_e32 v[54:55], 0
	v_mov_b64_e32 v[40:41], 0
	v_mov_b64_e32 v[42:43], 0
	v_mov_b64_e32 v[32:33], 0
	v_mov_b64_e32 v[34:35], 0

.LBB0_3584:
	s_ashr_i32 s21, s20, 31
	s_lshl_b64 s[22:23], s[20:21], 17
	s_add_u32 s22, s51, s22
	s_addc_u32 s23, s52, s23
	s_and_b64 s[24:25], s[2:3], exec
	s_cselect_b32 s21, s23, s31
	s_cselect_b32 s69, s22, s30
	s_ashr_i32 s17, s16, 31
	s_lshl_b64 s[24:25], s[16:17], 17
	s_add_u32 s24, s53, s24
	s_addc_u32 s25, s54, s25
	s_and_b64 s[34:35], s[2:3], exec
	v_mov_b32_e32 v0, 0
	s_cselect_b32 s17, s25, s29
	s_cselect_b32 s70, s24, s28
	s_mov_b64 s[38:39], 0
	s_mov_b64 s[34:35], -1
	s_mov_b64 s[36:37], 0
	v_mov_b32_e32 v1, v0
	v_mov_b64_e32 v[2:3], 0
	v_mov_b64_e32 v[4:5], 0
	v_mov_b64_e32 v[6:7], 0
	v_mov_b64_e32 v[28:29], 0
	v_mov_b64_e32 v[30:31], 0
	v_mov_b64_e32 v[40:41], 0
	v_mov_b64_e32 v[42:43], 0
	v_mov_b64_e32 v[48:49], 0
	v_mov_b64_e32 v[50:51], 0
	v_mov_b64_e32 v[52:53], 0
	v_mov_b64_e32 v[54:55], 0
	v_mov_b64_e32 v[72:73], 0
	v_mov_b64_e32 v[74:75], 0
	v_mov_b64_e32 v[80:81], 0
	v_mov_b64_e32 v[82:83], 0
	v_mov_b64_e32 v[88:89], 0
	v_mov_b64_e32 v[90:91], 0
	v_mov_b64_e32 v[96:97], 0
	v_mov_b64_e32 v[98:99], 0
	v_mov_b64_e32 v[104:105], 0
	v_mov_b64_e32 v[106:107], 0
	v_mov_b64_e32 v[112:113], 0
	v_mov_b64_e32 v[114:115], 0
	v_mov_b64_e32 v[76:77], 0
	v_mov_b64_e32 v[78:79], 0
	v_mov_b64_e32 v[84:85], 0
	v_mov_b64_e32 v[86:87], 0
	v_mov_b64_e32 v[92:93], 0
	v_mov_b64_e32 v[94:95], 0
	v_mov_b64_e32 v[100:101], 0
	v_mov_b64_e32 v[102:103], 0
	v_mov_b64_e32 v[108:109], 0
	v_mov_b64_e32 v[110:111], 0
	v_mov_b64_e32 v[116:117], 0
	v_mov_b64_e32 v[118:119], 0
	v_mov_b64_e32 v[120:121], 0
	v_mov_b64_e32 v[122:123], 0
	v_mov_b64_e32 v[124:125], 0
	v_mov_b64_e32 v[126:127], 0
	v_mov_b64_e32 v[32:33], 0
	v_mov_b64_e32 v[34:35], 0
	v_mov_b64_e32 v[24:25], 0
	v_mov_b64_e32 v[26:27], 0
	v_mov_b64_e32 v[12:13], 0
	v_mov_b64_e32 v[14:15], 0
	v_mov_b64_e32 v[8:9], 0
	v_mov_b64_e32 v[10:11], 0
	v_mov_b64_e32 v[68:69], 0
	v_mov_b64_e32 v[70:71], 0
	v_mov_b64_e32 v[64:65], 0
	v_mov_b64_e32 v[66:67], 0
	v_mov_b64_e32 v[60:61], 0
	v_mov_b64_e32 v[62:63], 0
	v_mov_b64_e32 v[56:57], 0
	v_mov_b64_e32 v[58:59], 0
	v_mov_b64_e32 v[44:45], 0
	v_mov_b64_e32 v[46:47], 0
	v_mov_b64_e32 v[36:37], 0
	v_mov_b64_e32 v[38:39], 0
	v_mov_b64_e32 v[20:21], 0
	v_mov_b64_e32 v[22:23], 0
	v_mov_b64_e32 v[16:17], 0
	v_mov_b64_e32 v[18:19], 0

.LBB0_3620:
	s_ashr_i32 s23, s22, 31
	s_lshl_b64 s[26:27], s[22:23], 19
	s_add_u32 s26, s18, s26
	s_addc_u32 s27, s19, s27
	s_and_b64 s[28:29], s[24:25], exec
	s_cselect_b32 s3, s27, s35
	s_cselect_b32 s23, s26, s34
	s_ashr_i32 s21, s20, 31
	s_lshl_b64 s[28:29], s[20:21], 19
	s_add_u32 s28, s33, s28
	s_addc_u32 s29, s40, s29
	s_and_b64 s[38:39], s[24:25], exec
	s_cselect_b32 s21, s29, s37
	s_cselect_b32 s52, s28, s36
	s_add_u32 s34, s34, 0x40080
	s_addc_u32 s35, s35, 0
	s_add_u32 s53, s36, 0x100
	v_mov_b32_e32 v36, 0
	s_addc_u32 s54, s37, 0
	s_mov_b32 s55, -2
	v_mov_b32_e32 v37, v36
	v_mov_b64_e32 v[38:39], 0
	v_mov_b64_e32 v[44:45], 0
	v_mov_b64_e32 v[46:47], 0
	v_mov_b64_e32 v[52:53], 0
	v_mov_b64_e32 v[54:55], 0
	v_mov_b64_e32 v[60:61], 0
	v_mov_b64_e32 v[62:63], 0
	v_mov_b64_e32 v[64:65], 0
	v_mov_b64_e32 v[66:67], 0
	v_mov_b64_e32 v[68:69], 0
	v_mov_b64_e32 v[70:71], 0
	v_mov_b64_e32 v[80:81], 0
	v_mov_b64_e32 v[82:83], 0
	v_mov_b64_e32 v[84:85], 0
	v_mov_b64_e32 v[86:87], 0
	v_mov_b64_e32 v[96:97], 0
	v_mov_b64_e32 v[98:99], 0
	v_mov_b64_e32 v[100:101], 0
	v_mov_b64_e32 v[102:103], 0
	v_mov_b64_e32 v[112:113], 0
	v_mov_b64_e32 v[114:115], 0
	v_mov_b64_e32 v[116:117], 0
	v_mov_b64_e32 v[118:119], 0
	v_mov_b64_e32 v[72:73], 0
	v_mov_b64_e32 v[74:75], 0
	v_mov_b64_e32 v[76:77], 0
	v_mov_b64_e32 v[78:79], 0
	v_mov_b64_e32 v[88:89], 0
	v_mov_b64_e32 v[90:91], 0
	v_mov_b64_e32 v[92:93], 0
	v_mov_b64_e32 v[94:95], 0
	v_mov_b64_e32 v[104:105], 0
	v_mov_b64_e32 v[106:107], 0
	v_mov_b64_e32 v[108:109], 0
	v_mov_b64_e32 v[110:111], 0
	v_mov_b64_e32 v[120:121], 0
	v_mov_b64_e32 v[122:123], 0
	v_mov_b64_e32 v[132:133], 0
	v_mov_b64_e32 v[134:135], 0
	v_mov_b64_e32 v[28:29], 0
	v_mov_b64_e32 v[30:31], 0
	v_mov_b64_e32 v[24:25], 0
	v_mov_b64_e32 v[26:27], 0
	v_mov_b64_e32 v[12:13], 0
	v_mov_b64_e32 v[14:15], 0
	v_mov_b64_e32 v[8:9], 0
	v_mov_b64_e32 v[10:11], 0
	v_mov_b64_e32 v[56:57], 0
	v_mov_b64_e32 v[58:59], 0
	v_mov_b64_e32 v[48:49], 0
	v_mov_b64_e32 v[50:51], 0
	v_mov_b64_e32 v[40:41], 0
	v_mov_b64_e32 v[42:43], 0
	s_waitcnt vmcnt(0)
	v_mov_b64_e32 v[32:33], 0
	v_mov_b64_e32 v[34:35], 0
	v_mov_b64_e32 v[20:21], 0
	v_mov_b64_e32 v[22:23], 0
	v_mov_b64_e32 v[16:17], 0
	v_mov_b64_e32 v[18:19], 0
	v_mov_b64_e32 v[4:5], 0
	v_mov_b64_e32 v[6:7], 0
	v_mov_b64_e32 v[0:1], 0
	v_mov_b64_e32 v[2:3], 0
